# all GEMM K loops: redundant s_setprio 1 + s_waitcnt lgkmcnt(0) removed from the head of every MFMA segment (right after the barrier)
# speedup vs baseline: 1.0059x; 1.0038x over previous
.LBB0_622:
	s_add_i32 s71, s60, 2
	s_add_u32 s7, s38, 0x80
	s_addc_u32 s10, s39, 0
	s_add_i32 s72, 0, 0x10000
	s_cmp_eq_u32 s64, s60
	s_cselect_b32 s61, s57, s10
	s_cselect_b32 s60, s56, s7
	s_cselect_b32 s11, s59, s63
	s_cselect_b32 s10, s58, s62
	s_add_i32 s7, 0, 0x14000
	v_add_u32_e32 v118, s72, v189
	v_add_u32_e32 v158, s7, v189
	ds_read_b128 v[106:109], v118
	ds_read_b128 v[110:113], v118 offset:1024
	ds_read_b128 v[114:117], v118 offset:2048
	ds_read_b128 v[118:121], v118 offset:3072
	ds_read_b128 v[146:149], v158
	ds_read_b128 v[150:153], v158 offset:1024
	ds_read_b128 v[154:157], v158 offset:2048
	ds_read_b128 v[158:161], v158 offset:3072
	v_lshl_add_u64 v[200:201], s[38:39], 0, v[168:169]
	s_add_i32 m0, s16, 0xc000
	ds_read_b128 v[172:175], v191
	ds_read_b128 v[176:179], v191 offset:1024
	ds_read_b128 v[180:183], v191 offset:2048
	ds_read_b128 v[192:195], v191 offset:3072
	ds_read_b128 v[196:199], v191 offset:4096
	ds_read_b128 v[210:213], v191 offset:5120
	ds_read_b128 v[214:217], v191 offset:6144
	ds_read_b128 v[218:221], v191 offset:7168
	global_load_lds_dwordx4 v[200:201], off
	v_lshl_add_u64 v[200:201], s[38:39], 0, v[170:171]
	s_add_i32 m0, s16, 0xe000
	s_nop 0
	global_load_lds_dwordx4 v[200:201], off
	s_waitcnt vmcnt(8)
	s_waitcnt lgkmcnt(0)
	s_setprio 1
	s_barrier
	v_mfma_f32_16x16x32_bf16 v[62:65], v[106:109], v[172:175], v[62:65]
	v_mfma_f32_16x16x32_bf16 v[58:61], v[114:117], v[172:175], v[58:61]
	v_mfma_f32_16x16x32_bf16 v[54:57], v[106:109], v[180:183], v[54:57]
	v_mfma_f32_16x16x32_bf16 v[50:53], v[114:117], v[180:183], v[50:53]
	v_mfma_f32_16x16x32_bf16 v[46:49], v[106:109], v[196:199], v[46:49]
	v_mfma_f32_16x16x32_bf16 v[42:45], v[114:117], v[196:199], v[42:45]
	v_mfma_f32_16x16x32_bf16 v[38:41], v[106:109], v[214:217], v[38:41]
	v_mfma_f32_16x16x32_bf16 v[34:37], v[114:117], v[214:217], v[34:37]
	v_mfma_f32_16x16x32_bf16 v[62:65], v[110:113], v[176:179], v[62:65]
	v_mfma_f32_16x16x32_bf16 v[58:61], v[118:121], v[176:179], v[58:61]
	v_mfma_f32_16x16x32_bf16 v[54:57], v[110:113], v[192:195], v[54:57]
	v_mfma_f32_16x16x32_bf16 v[50:53], v[118:121], v[192:195], v[50:53]
	v_mfma_f32_16x16x32_bf16 v[46:49], v[110:113], v[210:213], v[46:49]
	v_mfma_f32_16x16x32_bf16 v[42:45], v[118:121], v[210:213], v[42:45]
	v_mfma_f32_16x16x32_bf16 v[38:41], v[110:113], v[218:221], v[38:41]
	v_mfma_f32_16x16x32_bf16 v[34:37], v[118:121], v[218:221], v[34:37]
	s_setprio 0
	s_setprio 1
	v_mfma_f32_16x16x32_bf16 v[142:145], v[146:149], v[172:175], v[142:145]
	v_mfma_f32_16x16x32_bf16 v[138:141], v[154:157], v[172:175], v[138:141]
	v_mfma_f32_16x16x32_bf16 v[134:137], v[146:149], v[180:183], v[134:137]
	v_mfma_f32_16x16x32_bf16 v[130:133], v[154:157], v[180:183], v[130:133]
	v_mfma_f32_16x16x32_bf16 v[126:129], v[146:149], v[196:199], v[126:129]
	v_mfma_f32_16x16x32_bf16 v[122:125], v[154:157], v[196:199], v[122:125]
	v_mfma_f32_16x16x32_bf16 v[102:105], v[146:149], v[214:217], v[102:105]
	v_mfma_f32_16x16x32_bf16 v[98:101], v[154:157], v[214:217], v[98:101]
	v_mfma_f32_16x16x32_bf16 v[142:145], v[150:153], v[176:179], v[142:145]
	v_mfma_f32_16x16x32_bf16 v[138:141], v[158:161], v[176:179], v[138:141]
	v_mfma_f32_16x16x32_bf16 v[134:137], v[150:153], v[192:195], v[134:137]
	v_mfma_f32_16x16x32_bf16 v[130:133], v[158:161], v[192:195], v[130:133]
	v_mfma_f32_16x16x32_bf16 v[126:129], v[150:153], v[210:213], v[126:129]
	v_mfma_f32_16x16x32_bf16 v[122:125], v[158:161], v[210:213], v[122:125]
	v_mfma_f32_16x16x32_bf16 v[102:105], v[150:153], v[218:221], v[102:105]
	v_mfma_f32_16x16x32_bf16 v[98:101], v[158:161], v[218:221], v[98:101]
	s_setprio 0
	s_barrier
	s_add_i32 s72, s72, s13
	v_lshl_add_u64 v[200:201], s[10:11], 0, v[0:1]
	s_mov_b32 m0, s72
	ds_read_b128 v[172:175], v191 offset:16384
	ds_read_b128 v[176:179], v191 offset:17408
	ds_read_b128 v[180:183], v191 offset:18432
	ds_read_b128 v[192:195], v191 offset:19456
	ds_read_b128 v[196:199], v191 offset:20480
	ds_read_b128 v[210:213], v191 offset:21504
	ds_read_b128 v[214:217], v191 offset:22528
	ds_read_b128 v[218:221], v191 offset:23552
	global_load_lds_dwordx4 v[200:201], off
	s_add_i32 m0, s72, 0x2000
	v_lshl_add_u64 v[222:223], s[10:11], 0, v[166:167]
	s_add_u32 s10, s10, s0
	s_addc_u32 s11, s11, s1
	s_add_i32 s7, s7, s13
	global_load_lds_dwordx4 v[222:223], off
	v_lshl_add_u64 v[224:225], s[10:11], 0, v[0:1]
	s_mov_b32 m0, s7
	v_lshl_add_u64 v[226:227], s[10:11], 0, v[166:167]
	global_load_lds_dwordx4 v[224:225], off
	s_add_i32 m0, s7, 0x2000
	v_lshl_add_u64 v[228:229], s[60:61], 0, v[162:163]
	global_load_lds_dwordx4 v[226:227], off
	s_mov_b32 m0, s16
	v_lshl_add_u64 v[230:231], s[60:61], 0, v[164:165]
	global_load_lds_dwordx4 v[228:229], off
	s_mov_b32 m0, s17
	s_nop 0
	global_load_lds_dwordx4 v[230:231], off
	s_waitcnt vmcnt(8)
	s_waitcnt lgkmcnt(0)
	s_setprio 1
	s_barrier
	v_mfma_f32_16x16x32_bf16 v[30:33], v[106:109], v[172:175], v[30:33]
	v_mfma_f32_16x16x32_bf16 v[26:29], v[114:117], v[172:175], v[26:29]
	v_mfma_f32_16x16x32_bf16 v[22:25], v[106:109], v[180:183], v[22:25]
	v_mfma_f32_16x16x32_bf16 v[18:21], v[114:117], v[180:183], v[18:21]
	v_mfma_f32_16x16x32_bf16 v[14:17], v[106:109], v[196:199], v[14:17]
	v_mfma_f32_16x16x32_bf16 v[10:13], v[114:117], v[196:199], v[10:13]
	v_mfma_f32_16x16x32_bf16 v[6:9], v[106:109], v[214:217], v[6:9]
	v_mfma_f32_16x16x32_bf16 v[2:5], v[114:117], v[214:217], v[2:5]
	v_mfma_f32_16x16x32_bf16 v[30:33], v[110:113], v[176:179], v[30:33]
	v_mfma_f32_16x16x32_bf16 v[26:29], v[118:121], v[176:179], v[26:29]
	v_mfma_f32_16x16x32_bf16 v[22:25], v[110:113], v[192:195], v[22:25]
	v_mfma_f32_16x16x32_bf16 v[18:21], v[118:121], v[192:195], v[18:21]
	v_mfma_f32_16x16x32_bf16 v[14:17], v[110:113], v[210:213], v[14:17]
	v_mfma_f32_16x16x32_bf16 v[10:13], v[118:121], v[210:213], v[10:13]
	v_mfma_f32_16x16x32_bf16 v[6:9], v[110:113], v[218:221], v[6:9]
	v_mfma_f32_16x16x32_bf16 v[2:5], v[118:121], v[218:221], v[2:5]
	s_setprio 0
	s_setprio 1
	v_mfma_f32_16x16x32_bf16 v[94:97], v[146:149], v[172:175], v[94:97]
	v_mfma_f32_16x16x32_bf16 v[90:93], v[154:157], v[172:175], v[90:93]
	v_mfma_f32_16x16x32_bf16 v[86:89], v[146:149], v[180:183], v[86:89]
	v_mfma_f32_16x16x32_bf16 v[82:85], v[154:157], v[180:183], v[82:85]
	v_mfma_f32_16x16x32_bf16 v[78:81], v[146:149], v[196:199], v[78:81]
	v_mfma_f32_16x16x32_bf16 v[74:77], v[154:157], v[196:199], v[74:77]
	v_mfma_f32_16x16x32_bf16 v[70:73], v[146:149], v[214:217], v[70:73]
	v_mfma_f32_16x16x32_bf16 v[66:69], v[154:157], v[214:217], v[66:69]
	v_mfma_f32_16x16x32_bf16 v[94:97], v[150:153], v[176:179], v[94:97]
	v_mfma_f32_16x16x32_bf16 v[90:93], v[158:161], v[176:179], v[90:93]
	v_mfma_f32_16x16x32_bf16 v[86:89], v[150:153], v[192:195], v[86:89]
	v_mfma_f32_16x16x32_bf16 v[82:85], v[158:161], v[192:195], v[82:85]
	v_mfma_f32_16x16x32_bf16 v[78:81], v[150:153], v[210:213], v[78:81]
	v_mfma_f32_16x16x32_bf16 v[74:77], v[158:161], v[210:213], v[74:77]
	v_mfma_f32_16x16x32_bf16 v[70:73], v[150:153], v[218:221], v[70:73]
	v_mfma_f32_16x16x32_bf16 v[66:69], v[158:161], v[218:221], v[66:69]
	s_setprio 0
	s_barrier
	s_add_i32 s7, 0, 0x18000
	s_add_i32 s72, 0, 0x1c000
	v_add_u32_e32 v118, s7, v189
	v_add_u32_e32 v158, s72, v189
	ds_read_b128 v[106:109], v118
	ds_read_b128 v[110:113], v118 offset:1024
	ds_read_b128 v[114:117], v118 offset:2048
	ds_read_b128 v[118:121], v118 offset:3072
	ds_read_b128 v[146:149], v158
	ds_read_b128 v[150:153], v158 offset:1024
	ds_read_b128 v[154:157], v158 offset:2048
	ds_read_b128 v[158:161], v158 offset:3072
	s_add_u32 s10, s60, s0
	s_addc_u32 s11, s61, s1
	s_mov_b32 m0, s23
	v_lshl_add_u64 v[246:247], s[10:11], 0, v[162:163]
	ds_read_b128 v[172:175], v191 offset:32768
	ds_read_b128 v[176:179], v191 offset:33792
	ds_read_b128 v[180:183], v191 offset:34816
	ds_read_b128 v[192:195], v191 offset:35840
	ds_read_b128 v[196:199], v191 offset:36864
	ds_read_b128 v[210:213], v191 offset:37888
	ds_read_b128 v[214:217], v191 offset:38912
	ds_read_b128 v[218:221], v191 offset:39936
	global_load_lds_dwordx4 v[246:247], off
	v_lshl_add_u64 v[246:247], s[10:11], 0, v[164:165]
	s_mov_b32 m0, s26
	s_nop 0
	global_load_lds_dwordx4 v[246:247], off
	s_waitcnt vmcnt(8)
	s_waitcnt lgkmcnt(0)
	s_setprio 1
	s_barrier
	v_mfma_f32_16x16x32_bf16 v[62:65], v[106:109], v[172:175], v[62:65]
	v_mfma_f32_16x16x32_bf16 v[58:61], v[114:117], v[172:175], v[58:61]
	v_mfma_f32_16x16x32_bf16 v[54:57], v[106:109], v[180:183], v[54:57]
	v_mfma_f32_16x16x32_bf16 v[50:53], v[114:117], v[180:183], v[50:53]
	v_mfma_f32_16x16x32_bf16 v[46:49], v[106:109], v[196:199], v[46:49]
	v_mfma_f32_16x16x32_bf16 v[42:45], v[114:117], v[196:199], v[42:45]
	v_mfma_f32_16x16x32_bf16 v[38:41], v[106:109], v[214:217], v[38:41]
	v_mfma_f32_16x16x32_bf16 v[34:37], v[114:117], v[214:217], v[34:37]
	v_mfma_f32_16x16x32_bf16 v[62:65], v[110:113], v[176:179], v[62:65]
	v_mfma_f32_16x16x32_bf16 v[58:61], v[118:121], v[176:179], v[58:61]
	v_mfma_f32_16x16x32_bf16 v[54:57], v[110:113], v[192:195], v[54:57]
	v_mfma_f32_16x16x32_bf16 v[50:53], v[118:121], v[192:195], v[50:53]
	v_mfma_f32_16x16x32_bf16 v[46:49], v[110:113], v[210:213], v[46:49]
	v_mfma_f32_16x16x32_bf16 v[42:45], v[118:121], v[210:213], v[42:45]
	v_mfma_f32_16x16x32_bf16 v[38:41], v[110:113], v[218:221], v[38:41]
	v_mfma_f32_16x16x32_bf16 v[34:37], v[118:121], v[218:221], v[34:37]
	s_setprio 0
	s_setprio 1
	v_mfma_f32_16x16x32_bf16 v[142:145], v[146:149], v[172:175], v[142:145]
	v_mfma_f32_16x16x32_bf16 v[138:141], v[154:157], v[172:175], v[138:141]
	v_mfma_f32_16x16x32_bf16 v[134:137], v[146:149], v[180:183], v[134:137]
	v_mfma_f32_16x16x32_bf16 v[130:133], v[154:157], v[180:183], v[130:133]
	v_mfma_f32_16x16x32_bf16 v[126:129], v[146:149], v[196:199], v[126:129]
	v_mfma_f32_16x16x32_bf16 v[122:125], v[154:157], v[196:199], v[122:125]
	v_mfma_f32_16x16x32_bf16 v[102:105], v[146:149], v[214:217], v[102:105]
	v_mfma_f32_16x16x32_bf16 v[98:101], v[154:157], v[214:217], v[98:101]
	v_mfma_f32_16x16x32_bf16 v[142:145], v[150:153], v[176:179], v[142:145]
	v_mfma_f32_16x16x32_bf16 v[138:141], v[158:161], v[176:179], v[138:141]
	v_mfma_f32_16x16x32_bf16 v[134:137], v[150:153], v[192:195], v[134:137]
	v_mfma_f32_16x16x32_bf16 v[130:133], v[158:161], v[192:195], v[130:133]
	v_mfma_f32_16x16x32_bf16 v[126:129], v[150:153], v[210:213], v[126:129]
	v_mfma_f32_16x16x32_bf16 v[122:125], v[158:161], v[210:213], v[122:125]
	v_mfma_f32_16x16x32_bf16 v[102:105], v[150:153], v[218:221], v[102:105]
	v_mfma_f32_16x16x32_bf16 v[98:101], v[158:161], v[218:221], v[98:101]
	s_setprio 0
	s_barrier
	s_add_i32 s7, s7, s13
	v_lshl_add_u64 v[200:201], v[200:201], 0, s[14:15]
	s_mov_b32 m0, s7
	ds_read_b128 v[172:175], v191 offset:49152
	ds_read_b128 v[176:179], v191 offset:50176
	ds_read_b128 v[180:183], v191 offset:51200
	ds_read_b128 v[192:195], v191 offset:52224
	ds_read_b128 v[196:199], v191 offset:53248
	ds_read_b128 v[210:213], v191 offset:54272
	ds_read_b128 v[214:217], v191 offset:55296
	ds_read_b128 v[218:221], v191 offset:56320
	global_load_lds_dwordx4 v[200:201], off
	v_lshl_add_u64 v[200:201], v[222:223], 0, s[14:15]
	s_add_i32 m0, s7, 0x2000
	s_add_i32 s7, s72, s13
	global_load_lds_dwordx4 v[200:201], off
	v_lshl_add_u64 v[200:201], v[224:225], 0, s[14:15]
	s_mov_b32 m0, s7
	s_nop 0
	global_load_lds_dwordx4 v[200:201], off
	v_lshl_add_u64 v[200:201], v[226:227], 0, s[14:15]
	s_add_i32 m0, s7, 0x2000
	s_nop 0
	global_load_lds_dwordx4 v[200:201], off
	v_lshl_add_u64 v[200:201], v[228:229], 0, s[14:15]
	s_mov_b32 m0, s27
	s_nop 0
	global_load_lds_dwordx4 v[200:201], off
	v_lshl_add_u64 v[200:201], v[230:231], 0, s[14:15]
	s_mov_b32 m0, s28
	s_nop 0
	global_load_lds_dwordx4 v[200:201], off
	s_waitcnt vmcnt(8)
	s_waitcnt lgkmcnt(0)
	s_setprio 1
	s_barrier
	v_mfma_f32_16x16x32_bf16 v[30:33], v[106:109], v[172:175], v[30:33]
	v_mfma_f32_16x16x32_bf16 v[26:29], v[114:117], v[172:175], v[26:29]
	v_mfma_f32_16x16x32_bf16 v[22:25], v[106:109], v[180:183], v[22:25]
	v_mfma_f32_16x16x32_bf16 v[18:21], v[114:117], v[180:183], v[18:21]
	v_mfma_f32_16x16x32_bf16 v[14:17], v[106:109], v[196:199], v[14:17]
	v_mfma_f32_16x16x32_bf16 v[10:13], v[114:117], v[196:199], v[10:13]
	v_mfma_f32_16x16x32_bf16 v[6:9], v[106:109], v[214:217], v[6:9]
	v_mfma_f32_16x16x32_bf16 v[2:5], v[114:117], v[214:217], v[2:5]
	v_mfma_f32_16x16x32_bf16 v[30:33], v[110:113], v[176:179], v[30:33]
	v_mfma_f32_16x16x32_bf16 v[26:29], v[118:121], v[176:179], v[26:29]
	v_mfma_f32_16x16x32_bf16 v[22:25], v[110:113], v[192:195], v[22:25]
	v_mfma_f32_16x16x32_bf16 v[18:21], v[118:121], v[192:195], v[18:21]
	v_mfma_f32_16x16x32_bf16 v[14:17], v[110:113], v[210:213], v[14:17]
	v_mfma_f32_16x16x32_bf16 v[10:13], v[118:121], v[210:213], v[10:13]
	v_mfma_f32_16x16x32_bf16 v[6:9], v[110:113], v[218:221], v[6:9]
	v_mfma_f32_16x16x32_bf16 v[2:5], v[118:121], v[218:221], v[2:5]
	s_setprio 0
	s_setprio 1
	v_mfma_f32_16x16x32_bf16 v[94:97], v[146:149], v[172:175], v[94:97]
	v_mfma_f32_16x16x32_bf16 v[90:93], v[154:157], v[172:175], v[90:93]
	v_mfma_f32_16x16x32_bf16 v[86:89], v[146:149], v[180:183], v[86:89]
	v_mfma_f32_16x16x32_bf16 v[82:85], v[154:157], v[180:183], v[82:85]
	v_mfma_f32_16x16x32_bf16 v[78:81], v[146:149], v[196:199], v[78:81]
	v_mfma_f32_16x16x32_bf16 v[74:77], v[154:157], v[196:199], v[74:77]
	v_mfma_f32_16x16x32_bf16 v[70:73], v[146:149], v[214:217], v[70:73]
	v_mfma_f32_16x16x32_bf16 v[66:69], v[154:157], v[214:217], v[66:69]
	v_mfma_f32_16x16x32_bf16 v[94:97], v[150:153], v[176:179], v[94:97]
	v_mfma_f32_16x16x32_bf16 v[90:93], v[158:161], v[176:179], v[90:93]
	v_mfma_f32_16x16x32_bf16 v[86:89], v[150:153], v[192:195], v[86:89]
	v_mfma_f32_16x16x32_bf16 v[82:85], v[158:161], v[192:195], v[82:85]
	v_mfma_f32_16x16x32_bf16 v[78:81], v[150:153], v[210:213], v[78:81]
	v_mfma_f32_16x16x32_bf16 v[74:77], v[158:161], v[210:213], v[74:77]
	v_mfma_f32_16x16x32_bf16 v[70:73], v[150:153], v[218:221], v[70:73]
	v_mfma_f32_16x16x32_bf16 v[66:69], v[158:161], v[218:221], v[66:69]
	s_setprio 0
	s_barrier
	s_add_u32 s38, s38, 0x100
	s_addc_u32 s39, s39, 0
	s_add_u32 s62, s62, 0x100
	s_addc_u32 s63, s63, 0
	s_cmp_ge_i32 s71, s29
	s_mov_b32 s60, s71
	s_cbranch_scc0 .LBB0_622
	v_readlane_b32 s72, v255, 33
	v_readlane_b32 s73, v255, 34

.LBB0_702:
	s_waitcnt lgkmcnt(0)
	s_barrier
	s_setprio 1
	v_mfma_f32_16x16x128_f8f6f4 v[134:137], v[38:43], v[68:73], v[134:137] cbsz:2 blgp:2
	v_mfma_f32_16x16x128_f8f6f4 v[130:133], v[26:31], v[68:73], v[130:133] cbsz:2 blgp:2
	v_mfma_f32_16x16x128_f8f6f4 v[126:129], v[38:43], v[62:67], v[126:129] cbsz:2 blgp:2
	v_mfma_f32_16x16x128_f8f6f4 v[122:125], v[26:31], v[62:67], v[122:125] cbsz:2 blgp:2
	v_mfma_f32_16x16x128_f8f6f4 v[118:121], v[38:43], v[56:61], v[118:121] cbsz:2 blgp:2
	v_mfma_f32_16x16x128_f8f6f4 v[114:117], v[26:31], v[56:61], v[114:117] cbsz:2 blgp:2
	v_mfma_f32_16x16x128_f8f6f4 v[110:113], v[38:43], v[50:55], v[110:113] cbsz:2 blgp:2
	v_mfma_f32_16x16x128_f8f6f4 v[106:109], v[26:31], v[50:55], v[106:109] cbsz:2 blgp:2
	v_mfma_f32_16x16x128_f8f6f4 v[198:201], v[8:13], v[68:73], v[198:201] cbsz:2 blgp:2
	v_mfma_f32_16x16x128_f8f6f4 v[194:197], v[2:7], v[68:73], v[194:197] cbsz:2 blgp:2
	v_mfma_f32_16x16x128_f8f6f4 v[190:193], v[8:13], v[62:67], v[190:193] cbsz:2 blgp:2
	v_mfma_f32_16x16x128_f8f6f4 v[186:189], v[2:7], v[62:67], v[186:189] cbsz:2 blgp:2
	v_mfma_f32_16x16x128_f8f6f4 v[182:185], v[8:13], v[56:61], v[182:185] cbsz:2 blgp:2
	v_mfma_f32_16x16x128_f8f6f4 v[178:181], v[2:7], v[56:61], v[178:181] cbsz:2 blgp:2
	v_mfma_f32_16x16x128_f8f6f4 v[174:177], v[8:13], v[50:55], v[174:177] cbsz:2 blgp:2
	v_mfma_f32_16x16x128_f8f6f4 v[170:173], v[2:7], v[50:55], v[170:173] cbsz:2 blgp:2
	v_mfma_f32_16x16x128_f8f6f4 v[102:105], v[38:43], v[44:49], v[102:105] cbsz:2 blgp:2
	v_mfma_f32_16x16x128_f8f6f4 v[98:101], v[26:31], v[44:49], v[98:101] cbsz:2 blgp:2
	v_mfma_f32_16x16x128_f8f6f4 v[94:97], v[38:43], v[32:37], v[94:97] cbsz:2 blgp:2
	v_mfma_f32_16x16x128_f8f6f4 v[90:93], v[26:31], v[32:37], v[90:93] cbsz:2 blgp:2
	v_mfma_f32_16x16x128_f8f6f4 v[86:89], v[38:43], v[20:25], v[86:89] cbsz:2 blgp:2
	v_mfma_f32_16x16x128_f8f6f4 v[82:85], v[26:31], v[20:25], v[82:85] cbsz:2 blgp:2
	v_mfma_f32_16x16x128_f8f6f4 v[78:81], v[38:43], v[14:19], v[78:81] cbsz:2 blgp:2
	v_mfma_f32_16x16x128_f8f6f4 v[74:77], v[26:31], v[14:19], v[74:77] cbsz:2 blgp:2
	v_mfma_f32_16x16x128_f8f6f4 v[166:169], v[8:13], v[44:49], v[166:169] cbsz:2 blgp:2
	v_mfma_f32_16x16x128_f8f6f4 v[162:165], v[2:7], v[44:49], v[162:165] cbsz:2 blgp:2
	v_mfma_f32_16x16x128_f8f6f4 v[158:161], v[8:13], v[32:37], v[158:161] cbsz:2 blgp:2
	v_mfma_f32_16x16x128_f8f6f4 v[154:157], v[2:7], v[32:37], v[154:157] cbsz:2 blgp:2
	v_mfma_f32_16x16x128_f8f6f4 v[150:153], v[8:13], v[20:25], v[150:153] cbsz:2 blgp:2
	v_mfma_f32_16x16x128_f8f6f4 v[146:149], v[2:7], v[20:25], v[146:149] cbsz:2 blgp:2
	v_mfma_f32_16x16x128_f8f6f4 v[142:145], v[8:13], v[14:19], v[142:145] cbsz:2 blgp:2
	v_mfma_f32_16x16x128_f8f6f4 v[138:141], v[2:7], v[14:19], v[138:141] cbsz:2 blgp:2
	s_setprio 0
	s_andn2_b64 vcc, exec, s[54:55]
	s_cbranch_vccnz .LBB0_699
	s_waitcnt vmcnt(6)
	s_branch .LBB0_699

.LBB0_786:
	s_waitcnt lgkmcnt(0)
	s_barrier
	s_setprio 1
	v_mfma_f32_16x16x128_f8f6f4 v[134:137], v[38:43], v[68:73], v[134:137] cbsz:2 blgp:2
	v_mfma_f32_16x16x128_f8f6f4 v[130:133], v[26:31], v[68:73], v[130:133] cbsz:2 blgp:2
	v_mfma_f32_16x16x128_f8f6f4 v[126:129], v[38:43], v[62:67], v[126:129] cbsz:2 blgp:2
	v_mfma_f32_16x16x128_f8f6f4 v[122:125], v[26:31], v[62:67], v[122:125] cbsz:2 blgp:2
	v_mfma_f32_16x16x128_f8f6f4 v[118:121], v[38:43], v[56:61], v[118:121] cbsz:2 blgp:2
	v_mfma_f32_16x16x128_f8f6f4 v[114:117], v[26:31], v[56:61], v[114:117] cbsz:2 blgp:2
	v_mfma_f32_16x16x128_f8f6f4 v[110:113], v[38:43], v[50:55], v[110:113] cbsz:2 blgp:2
	v_mfma_f32_16x16x128_f8f6f4 v[106:109], v[26:31], v[50:55], v[106:109] cbsz:2 blgp:2
	v_mfma_f32_16x16x128_f8f6f4 v[198:201], v[8:13], v[68:73], v[198:201] cbsz:2 blgp:2
	v_mfma_f32_16x16x128_f8f6f4 v[194:197], v[2:7], v[68:73], v[194:197] cbsz:2 blgp:2
	v_mfma_f32_16x16x128_f8f6f4 v[190:193], v[8:13], v[62:67], v[190:193] cbsz:2 blgp:2
	v_mfma_f32_16x16x128_f8f6f4 v[186:189], v[2:7], v[62:67], v[186:189] cbsz:2 blgp:2
	v_mfma_f32_16x16x128_f8f6f4 v[182:185], v[8:13], v[56:61], v[182:185] cbsz:2 blgp:2
	v_mfma_f32_16x16x128_f8f6f4 v[178:181], v[2:7], v[56:61], v[178:181] cbsz:2 blgp:2
	v_mfma_f32_16x16x128_f8f6f4 v[174:177], v[8:13], v[50:55], v[174:177] cbsz:2 blgp:2
	v_mfma_f32_16x16x128_f8f6f4 v[170:173], v[2:7], v[50:55], v[170:173] cbsz:2 blgp:2
	v_mfma_f32_16x16x128_f8f6f4 v[102:105], v[38:43], v[44:49], v[102:105] cbsz:2 blgp:2
	v_mfma_f32_16x16x128_f8f6f4 v[98:101], v[26:31], v[44:49], v[98:101] cbsz:2 blgp:2
	v_mfma_f32_16x16x128_f8f6f4 v[94:97], v[38:43], v[32:37], v[94:97] cbsz:2 blgp:2
	v_mfma_f32_16x16x128_f8f6f4 v[90:93], v[26:31], v[32:37], v[90:93] cbsz:2 blgp:2
	v_mfma_f32_16x16x128_f8f6f4 v[86:89], v[38:43], v[20:25], v[86:89] cbsz:2 blgp:2
	v_mfma_f32_16x16x128_f8f6f4 v[82:85], v[26:31], v[20:25], v[82:85] cbsz:2 blgp:2
	v_mfma_f32_16x16x128_f8f6f4 v[78:81], v[38:43], v[14:19], v[78:81] cbsz:2 blgp:2
	v_mfma_f32_16x16x128_f8f6f4 v[74:77], v[26:31], v[14:19], v[74:77] cbsz:2 blgp:2
	v_mfma_f32_16x16x128_f8f6f4 v[166:169], v[8:13], v[44:49], v[166:169] cbsz:2 blgp:2
	v_mfma_f32_16x16x128_f8f6f4 v[162:165], v[2:7], v[44:49], v[162:165] cbsz:2 blgp:2
	v_mfma_f32_16x16x128_f8f6f4 v[158:161], v[8:13], v[32:37], v[158:161] cbsz:2 blgp:2
	v_mfma_f32_16x16x128_f8f6f4 v[154:157], v[2:7], v[32:37], v[154:157] cbsz:2 blgp:2
	v_mfma_f32_16x16x128_f8f6f4 v[150:153], v[8:13], v[20:25], v[150:153] cbsz:2 blgp:2
	v_mfma_f32_16x16x128_f8f6f4 v[146:149], v[2:7], v[20:25], v[146:149] cbsz:2 blgp:2
	v_mfma_f32_16x16x128_f8f6f4 v[142:145], v[8:13], v[14:19], v[142:145] cbsz:2 blgp:2
	v_mfma_f32_16x16x128_f8f6f4 v[138:141], v[2:7], v[14:19], v[138:141] cbsz:2 blgp:2
	s_setprio 0
	s_andn2_b64 vcc, exec, s[48:49]
	s_cbranch_vccnz .LBB0_783
	s_waitcnt vmcnt(6)
	s_branch .LBB0_783

.LBB0_1637:
	s_add_i32 s71, s70, 2
	s_add_u32 s7, s48, 0x80
	s_addc_u32 s10, s49, 0
	s_cmp_eq_u32 s60, s70
	s_cselect_b32 s51, s39, s10
	s_cselect_b32 s50, s38, s7
	s_cselect_b32 s53, s47, s69
	s_cselect_b32 s52, s46, s68
	s_add_i32 s7, 0, 0x10000
	v_add_u32_e32 v130, s7, v215
	s_add_i32 s70, 0, 0x14000
	ds_read_b128 v[134:137], v130
	ds_read_b128 v[138:141], v130 offset:1024
	ds_read_b128 v[142:145], v130 offset:2048
	ds_read_b128 v[146:149], v130 offset:3072
	v_add_u32_e32 v130, s70, v215
	ds_read_b128 v[150:153], v130
	ds_read_b128 v[154:157], v130 offset:1024
	ds_read_b128 v[158:161], v130 offset:2048
	ds_read_b128 v[162:165], v130 offset:3072
	v_lshl_add_u64 v[130:131], s[48:49], 0, v[200:201]
	s_add_i32 m0, s23, 0xc000
	ds_read_b128 v[166:169], v216
	ds_read_b128 v[170:173], v216 offset:1024
	ds_read_b128 v[174:177], v216 offset:2048
	ds_read_b128 v[178:181], v216 offset:3072
	ds_read_b128 v[182:185], v216 offset:4096
	ds_read_b128 v[186:189], v216 offset:5120
	ds_read_b128 v[218:221], v216 offset:6144
	ds_read_b128 v[222:225], v216 offset:7168
	global_load_lds_dwordx4 v[130:131], off
	v_lshl_add_u64 v[130:131], s[48:49], 0, v[210:211]
	s_add_i32 m0, s23, 0xe000
	s_nop 0
	global_load_lds_dwordx4 v[130:131], off
	s_waitcnt vmcnt(8)
	s_waitcnt lgkmcnt(0)
	s_setprio 1
	s_barrier
	v_mfma_f32_16x16x128_f8f6f4 v[126:129], v[134:141], v[166:173], v[126:129]
	v_mfma_f32_16x16x128_f8f6f4 v[122:125], v[142:149], v[166:173], v[122:125]
	v_mfma_f32_16x16x128_f8f6f4 v[110:113], v[134:141], v[174:181], v[110:113]
	v_mfma_f32_16x16x128_f8f6f4 v[106:109], v[142:149], v[174:181], v[106:109]
	v_mfma_f32_16x16x128_f8f6f4 v[94:97], v[134:141], v[182:189], v[94:97]
	v_mfma_f32_16x16x128_f8f6f4 v[90:93], v[142:149], v[182:189], v[90:93]
	v_mfma_f32_16x16x128_f8f6f4 v[78:81], v[134:141], v[218:225], v[78:81]
	v_mfma_f32_16x16x128_f8f6f4 v[74:77], v[142:149], v[218:225], v[74:77]
	s_setprio 0
	s_setprio 1
	v_mfma_f32_16x16x128_f8f6f4 v[118:121], v[150:157], v[166:173], v[118:121]
	v_mfma_f32_16x16x128_f8f6f4 v[114:117], v[158:165], v[166:173], v[114:117]
	v_mfma_f32_16x16x128_f8f6f4 v[102:105], v[150:157], v[174:181], v[102:105]
	v_mfma_f32_16x16x128_f8f6f4 v[98:101], v[158:165], v[174:181], v[98:101]
	v_mfma_f32_16x16x128_f8f6f4 v[86:89], v[150:157], v[182:189], v[86:89]
	v_mfma_f32_16x16x128_f8f6f4 v[82:85], v[158:165], v[182:189], v[82:85]
	v_mfma_f32_16x16x128_f8f6f4 v[70:73], v[150:157], v[218:225], v[70:73]
	v_mfma_f32_16x16x128_f8f6f4 v[66:69], v[158:165], v[218:225], v[66:69]
	s_setprio 0
	s_barrier
	s_add_i32 s7, s7, s17
	v_lshl_add_u64 v[130:131], s[52:53], 0, v[0:1]
	s_mov_b32 m0, s7
	ds_read_b128 v[166:169], v216 offset:16384
	ds_read_b128 v[170:173], v216 offset:17408
	ds_read_b128 v[174:177], v216 offset:18432
	ds_read_b128 v[178:181], v216 offset:19456
	ds_read_b128 v[182:185], v216 offset:20480
	ds_read_b128 v[186:189], v216 offset:21504
	ds_read_b128 v[218:221], v216 offset:22528
	ds_read_b128 v[222:225], v216 offset:23552
	global_load_lds_dwordx4 v[130:131], off
	s_add_i32 m0, s7, 0x2000
	s_add_u32 s10, s52, s0
	v_lshl_add_u64 v[132:133], s[52:53], 0, v[198:199]
	s_addc_u32 s11, s53, s1
	s_add_i32 s7, s70, s17
	global_load_lds_dwordx4 v[132:133], off
	v_lshl_add_u64 v[190:191], s[10:11], 0, v[0:1]
	s_mov_b32 m0, s7
	v_lshl_add_u64 v[192:193], s[10:11], 0, v[198:199]
	global_load_lds_dwordx4 v[190:191], off
	s_add_i32 m0, s7, 0x2000
	v_lshl_add_u64 v[212:213], s[50:51], 0, v[194:195]
	global_load_lds_dwordx4 v[192:193], off
	s_mov_b32 m0, s23
	v_lshl_add_u64 v[226:227], s[50:51], 0, v[196:197]
	global_load_lds_dwordx4 v[212:213], off
	s_mov_b32 m0, s26
	s_nop 0
	global_load_lds_dwordx4 v[226:227], off
	s_waitcnt vmcnt(8)
	s_waitcnt lgkmcnt(0)
	s_setprio 1
	s_barrier
	v_mfma_f32_16x16x128_f8f6f4 v[62:65], v[134:141], v[166:173], v[62:65]
	v_mfma_f32_16x16x128_f8f6f4 v[58:61], v[142:149], v[166:173], v[58:61]
	v_mfma_f32_16x16x128_f8f6f4 v[46:49], v[134:141], v[174:181], v[46:49]
	v_mfma_f32_16x16x128_f8f6f4 v[42:45], v[142:149], v[174:181], v[42:45]
	v_mfma_f32_16x16x128_f8f6f4 v[30:33], v[134:141], v[182:189], v[30:33]
	v_mfma_f32_16x16x128_f8f6f4 v[26:29], v[142:149], v[182:189], v[26:29]
	v_mfma_f32_16x16x128_f8f6f4 v[14:17], v[134:141], v[218:225], v[14:17]
	v_mfma_f32_16x16x128_f8f6f4 v[10:13], v[142:149], v[218:225], v[10:13]
	s_setprio 0
	s_setprio 1
	v_mfma_f32_16x16x128_f8f6f4 v[54:57], v[150:157], v[166:173], v[54:57]
	v_mfma_f32_16x16x128_f8f6f4 v[50:53], v[158:165], v[166:173], v[50:53]
	v_mfma_f32_16x16x128_f8f6f4 v[38:41], v[150:157], v[174:181], v[38:41]
	v_mfma_f32_16x16x128_f8f6f4 v[34:37], v[158:165], v[174:181], v[34:37]
	v_mfma_f32_16x16x128_f8f6f4 v[22:25], v[150:157], v[182:189], v[22:25]
	v_mfma_f32_16x16x128_f8f6f4 v[18:21], v[158:165], v[182:189], v[18:21]
	v_mfma_f32_16x16x128_f8f6f4 v[6:9], v[150:157], v[218:225], v[6:9]
	v_mfma_f32_16x16x128_f8f6f4 v[2:5], v[158:165], v[218:225], v[2:5]
	s_setprio 0
	s_barrier
	s_add_i32 s7, 0, 0x18000
	s_add_i32 s52, 0, 0x1c000
	v_add_u32_e32 v146, s7, v215
	v_add_u32_e32 v162, s52, v215
	ds_read_b128 v[134:137], v146
	ds_read_b128 v[138:141], v146 offset:1024
	ds_read_b128 v[142:145], v146 offset:2048
	ds_read_b128 v[146:149], v146 offset:3072
	ds_read_b128 v[150:153], v162
	ds_read_b128 v[154:157], v162 offset:1024
	ds_read_b128 v[158:161], v162 offset:2048
	ds_read_b128 v[162:165], v162 offset:3072
	s_add_u32 s10, s50, s0
	s_addc_u32 s11, s51, s1
	s_mov_b32 m0, s27
	v_lshl_add_u64 v[228:229], s[10:11], 0, v[194:195]
	ds_read_b128 v[166:169], v216 offset:32768
	ds_read_b128 v[170:173], v216 offset:33792
	ds_read_b128 v[174:177], v216 offset:34816
	ds_read_b128 v[178:181], v216 offset:35840
	ds_read_b128 v[182:185], v216 offset:36864
	ds_read_b128 v[186:189], v216 offset:37888
	ds_read_b128 v[218:221], v216 offset:38912
	ds_read_b128 v[222:225], v216 offset:39936
	global_load_lds_dwordx4 v[228:229], off
	v_lshl_add_u64 v[228:229], s[10:11], 0, v[196:197]
	s_mov_b32 m0, s54
	s_nop 0
	global_load_lds_dwordx4 v[228:229], off
	s_waitcnt vmcnt(8)
	s_waitcnt lgkmcnt(0)
	s_setprio 1
	s_barrier
	v_mfma_f32_16x16x128_f8f6f4 v[126:129], v[134:141], v[166:173], v[126:129]
	v_mfma_f32_16x16x128_f8f6f4 v[122:125], v[142:149], v[166:173], v[122:125]
	v_mfma_f32_16x16x128_f8f6f4 v[110:113], v[134:141], v[174:181], v[110:113]
	v_mfma_f32_16x16x128_f8f6f4 v[106:109], v[142:149], v[174:181], v[106:109]
	v_mfma_f32_16x16x128_f8f6f4 v[94:97], v[134:141], v[182:189], v[94:97]
	v_mfma_f32_16x16x128_f8f6f4 v[90:93], v[142:149], v[182:189], v[90:93]
	v_mfma_f32_16x16x128_f8f6f4 v[78:81], v[134:141], v[218:225], v[78:81]
	v_mfma_f32_16x16x128_f8f6f4 v[74:77], v[142:149], v[218:225], v[74:77]
	s_setprio 0
	s_setprio 1
	v_mfma_f32_16x16x128_f8f6f4 v[118:121], v[150:157], v[166:173], v[118:121]
	v_mfma_f32_16x16x128_f8f6f4 v[114:117], v[158:165], v[166:173], v[114:117]
	v_mfma_f32_16x16x128_f8f6f4 v[102:105], v[150:157], v[174:181], v[102:105]
	v_mfma_f32_16x16x128_f8f6f4 v[98:101], v[158:165], v[174:181], v[98:101]
	v_mfma_f32_16x16x128_f8f6f4 v[86:89], v[150:157], v[182:189], v[86:89]
	v_mfma_f32_16x16x128_f8f6f4 v[82:85], v[158:165], v[182:189], v[82:85]
	v_mfma_f32_16x16x128_f8f6f4 v[70:73], v[150:157], v[218:225], v[70:73]
	v_mfma_f32_16x16x128_f8f6f4 v[66:69], v[158:165], v[218:225], v[66:69]
	s_setprio 0
	s_barrier
	s_add_i32 s7, s7, s17
	v_lshl_add_u64 v[130:131], v[130:131], 0, s[14:15]
	s_mov_b32 m0, s7
	ds_read_b128 v[166:169], v216 offset:49152
	ds_read_b128 v[170:173], v216 offset:50176
	ds_read_b128 v[174:177], v216 offset:51200
	ds_read_b128 v[178:181], v216 offset:52224
	ds_read_b128 v[182:185], v216 offset:53248
	ds_read_b128 v[186:189], v216 offset:54272
	ds_read_b128 v[218:221], v216 offset:55296
	ds_read_b128 v[222:225], v216 offset:56320
	global_load_lds_dwordx4 v[130:131], off
	v_lshl_add_u64 v[130:131], v[132:133], 0, s[14:15]
	s_add_i32 m0, s7, 0x2000
	s_add_i32 s7, s52, s17
	global_load_lds_dwordx4 v[130:131], off
	v_lshl_add_u64 v[130:131], v[190:191], 0, s[14:15]
	s_mov_b32 m0, s7
	s_nop 0
	global_load_lds_dwordx4 v[130:131], off
	v_lshl_add_u64 v[130:131], v[192:193], 0, s[14:15]
	s_add_i32 m0, s7, 0x2000
	s_nop 0
	global_load_lds_dwordx4 v[130:131], off
	v_lshl_add_u64 v[130:131], v[212:213], 0, s[14:15]
	s_mov_b32 m0, s58
	s_nop 0
	global_load_lds_dwordx4 v[130:131], off
	v_lshl_add_u64 v[130:131], v[226:227], 0, s[14:15]
	s_mov_b32 m0, s59
	s_nop 0
	global_load_lds_dwordx4 v[130:131], off
	s_waitcnt vmcnt(8)
	s_waitcnt lgkmcnt(0)
	s_setprio 1
	s_barrier
	v_mfma_f32_16x16x128_f8f6f4 v[62:65], v[134:141], v[166:173], v[62:65]
	v_mfma_f32_16x16x128_f8f6f4 v[58:61], v[142:149], v[166:173], v[58:61]
	v_mfma_f32_16x16x128_f8f6f4 v[46:49], v[134:141], v[174:181], v[46:49]
	v_mfma_f32_16x16x128_f8f6f4 v[42:45], v[142:149], v[174:181], v[42:45]
	v_mfma_f32_16x16x128_f8f6f4 v[30:33], v[134:141], v[182:189], v[30:33]
	v_mfma_f32_16x16x128_f8f6f4 v[26:29], v[142:149], v[182:189], v[26:29]
	v_mfma_f32_16x16x128_f8f6f4 v[14:17], v[134:141], v[218:225], v[14:17]
	v_mfma_f32_16x16x128_f8f6f4 v[10:13], v[142:149], v[218:225], v[10:13]
	s_setprio 0
	s_setprio 1
	v_mfma_f32_16x16x128_f8f6f4 v[54:57], v[150:157], v[166:173], v[54:57]
	v_mfma_f32_16x16x128_f8f6f4 v[50:53], v[158:165], v[166:173], v[50:53]
	v_mfma_f32_16x16x128_f8f6f4 v[38:41], v[150:157], v[174:181], v[38:41]
	v_mfma_f32_16x16x128_f8f6f4 v[34:37], v[158:165], v[174:181], v[34:37]
	v_mfma_f32_16x16x128_f8f6f4 v[22:25], v[150:157], v[182:189], v[22:25]
	v_mfma_f32_16x16x128_f8f6f4 v[18:21], v[158:165], v[182:189], v[18:21]
	v_mfma_f32_16x16x128_f8f6f4 v[6:9], v[150:157], v[218:225], v[6:9]
	v_mfma_f32_16x16x128_f8f6f4 v[2:5], v[158:165], v[218:225], v[2:5]
	s_setprio 0
	s_barrier
	s_addk_i32 s8, 0x400
	s_add_u32 s48, s48, 0x100
	s_addc_u32 s49, s49, 0
	s_add_u32 s68, s68, 0x100
	s_addc_u32 s69, s69, 0
	s_cmp_ge_i32 s71, s55
	s_cbranch_scc1 .LBB0_1640
	s_mov_b32 s70, s71
	s_cmp_lt_i32 s70, 16
	s_cbranch_scc1 .LBB0_1633

.LBB0_1722:
	s_add_i32 vcc_hi, s66, 2
	s_add_u32 s10, s64, 0x80
	s_addc_u32 s11, s65, 0
	s_add_i32 s7, 0, 0x10000
	s_cmp_eq_u32 s74, s66
	s_cselect_b32 s67, s39, s11
	s_cselect_b32 s66, s38, s10
	s_cselect_b32 s69, s63, vcc_lo
	s_cselect_b32 s68, s62, s97
	s_add_i32 s10, 0, 0x14000
	v_add_u32_e32 v2, s7, v228
	v_add_u32_e32 v6, s10, v228
	ds_read_b128 v[26:29], v2
	ds_read_b128 v[30:33], v2 offset:1024
	ds_read_b128 v[18:21], v2 offset:2048
	ds_read_b128 v[22:25], v2 offset:3072
	ds_read_b128 v[10:13], v6
	ds_read_b128 v[14:17], v6 offset:1024
	s_waitcnt lgkmcnt(0)
	ds_read_b128 v[2:5], v6 offset:2048
	ds_read_b128 v[6:9], v6 offset:3072
	v_lshl_add_u64 v[196:197], s[64:65], 0, v[168:169]
	s_add_i32 m0, s16, 0xc000
	ds_read_b128 v[172:175], v229
	ds_read_b128 v[176:179], v229 offset:1024
	ds_read_b128 v[180:183], v229 offset:2048
	ds_read_b128 v[184:187], v229 offset:3072
	ds_read_b128 v[188:191], v229 offset:4096
	ds_read_b128 v[192:195], v229 offset:5120
	ds_read_b128 v[210:213], v229 offset:6144
	ds_read_b128 v[214:217], v229 offset:7168
	global_load_lds_dwordx4 v[196:197], off
	v_lshl_add_u64 v[196:197], s[64:65], 0, v[170:171]
	s_add_i32 m0, s16, 0xe000
	s_nop 0
	global_load_lds_dwordx4 v[196:197], off
	s_waitcnt vmcnt(8)
	s_waitcnt lgkmcnt(0)
	s_setprio 1
	s_barrier
	v_mfma_f32_16x16x128_f8f6f4 v[158:161], v[26:33], v[172:179], v[158:161]
	v_mfma_f32_16x16x128_f8f6f4 v[154:157], v[18:25], v[172:179], v[154:157]
	v_mfma_f32_16x16x128_f8f6f4 v[150:153], v[26:33], v[180:187], v[150:153]
	v_mfma_f32_16x16x128_f8f6f4 v[146:149], v[18:25], v[180:187], v[146:149]
	v_mfma_f32_16x16x128_f8f6f4 v[138:141], v[26:33], v[188:195], v[138:141]
	v_mfma_f32_16x16x128_f8f6f4 v[130:133], v[18:25], v[188:195], v[130:133]
	v_mfma_f32_16x16x128_f8f6f4 v[122:125], v[26:33], v[210:217], v[122:125]
	v_mfma_f32_16x16x128_f8f6f4 v[114:117], v[18:25], v[210:217], v[114:117]
	s_setprio 0
	s_setprio 1
	v_mfma_f32_16x16x128_f8f6f4 v[142:145], v[10:17], v[172:179], v[142:145]
	v_mfma_f32_16x16x128_f8f6f4 v[134:137], v[2:9], v[172:179], v[134:137]
	v_mfma_f32_16x16x128_f8f6f4 v[126:129], v[10:17], v[180:187], v[126:129]
	v_mfma_f32_16x16x128_f8f6f4 v[118:121], v[2:9], v[180:187], v[118:121]
	v_mfma_f32_16x16x128_f8f6f4 v[110:113], v[10:17], v[188:195], v[110:113]
	v_mfma_f32_16x16x128_f8f6f4 v[106:109], v[2:9], v[188:195], v[106:109]
	v_mfma_f32_16x16x128_f8f6f4 v[102:105], v[10:17], v[210:217], v[102:105]
	v_mfma_f32_16x16x128_f8f6f4 v[98:101], v[2:9], v[210:217], v[98:101]
	s_setprio 0
	s_barrier
	s_add_i32 s7, s7, s13
	v_lshl_add_u64 v[172:173], s[68:69], 0, v[0:1]
	s_mov_b32 m0, s7
	ds_read_b128 v[184:187], v229 offset:16384
	ds_read_b128 v[188:191], v229 offset:17408
	ds_read_b128 v[192:195], v229 offset:18432
	ds_read_b128 v[196:199], v229 offset:19456
	ds_read_b128 v[210:213], v229 offset:20480
	ds_read_b128 v[214:217], v229 offset:21504
	ds_read_b128 v[218:221], v229 offset:22528
	ds_read_b128 v[222:225], v229 offset:23552
	global_load_lds_dwordx4 v[172:173], off
	s_add_i32 m0, s7, 0x2000
	v_lshl_add_u64 v[174:175], s[68:69], 0, v[166:167]
	s_add_u32 s68, s68, s28
	s_addc_u32 s69, s69, s29
	s_add_i32 s7, s10, s13
	global_load_lds_dwordx4 v[174:175], off
	v_lshl_add_u64 v[176:177], s[68:69], 0, v[0:1]
	s_mov_b32 m0, s7
	v_lshl_add_u64 v[178:179], s[68:69], 0, v[166:167]
	global_load_lds_dwordx4 v[176:177], off
	s_add_i32 m0, s7, 0x2000
	v_lshl_add_u64 v[180:181], s[66:67], 0, v[162:163]
	global_load_lds_dwordx4 v[178:179], off
	s_mov_b32 m0, s16
	v_lshl_add_u64 v[182:183], s[66:67], 0, v[164:165]
	global_load_lds_dwordx4 v[180:181], off
	s_mov_b32 m0, s17
	s_nop 0
	global_load_lds_dwordx4 v[182:183], off
	s_waitcnt vmcnt(8)
	s_waitcnt lgkmcnt(0)
	s_setprio 1
	s_barrier
	v_mfma_f32_16x16x128_f8f6f4 v[94:97], v[26:33], v[184:191], v[94:97]
	v_mfma_f32_16x16x128_f8f6f4 v[90:93], v[18:25], v[184:191], v[90:93]
	v_mfma_f32_16x16x128_f8f6f4 v[86:89], v[26:33], v[192:199], v[86:89]
	v_mfma_f32_16x16x128_f8f6f4 v[82:85], v[18:25], v[192:199], v[82:85]
	v_mfma_f32_16x16x128_f8f6f4 v[74:77], v[26:33], v[210:217], v[74:77]
	v_mfma_f32_16x16x128_f8f6f4 v[66:69], v[18:25], v[210:217], v[66:69]
	v_mfma_f32_16x16x128_f8f6f4 v[58:61], v[26:33], v[218:225], v[58:61]
	v_mfma_f32_16x16x128_f8f6f4 v[50:53], v[18:25], v[218:225], v[50:53]
	s_setprio 0
	s_setprio 1
	v_mfma_f32_16x16x128_f8f6f4 v[78:81], v[10:17], v[184:191], v[78:81]
	v_mfma_f32_16x16x128_f8f6f4 v[70:73], v[2:9], v[184:191], v[70:73]
	v_mfma_f32_16x16x128_f8f6f4 v[62:65], v[10:17], v[192:199], v[62:65]
	v_mfma_f32_16x16x128_f8f6f4 v[54:57], v[2:9], v[192:199], v[54:57]
	v_mfma_f32_16x16x128_f8f6f4 v[46:49], v[10:17], v[210:217], v[46:49]
	v_mfma_f32_16x16x128_f8f6f4 v[42:45], v[2:9], v[210:217], v[42:45]
	v_mfma_f32_16x16x128_f8f6f4 v[38:41], v[10:17], v[218:225], v[38:41]
	v_mfma_f32_16x16x128_f8f6f4 v[34:37], v[2:9], v[218:225], v[34:37]
	s_setprio 0
	s_barrier
	s_add_i32 s7, 0, 0x18000
	s_add_i32 s68, 0, 0x1c000
	v_add_u32_e32 v14, s7, v228
	v_add_u32_e32 v30, s68, v228
	ds_read_b128 v[2:5], v14
	ds_read_b128 v[6:9], v14 offset:1024
	ds_read_b128 v[10:13], v14 offset:2048
	ds_read_b128 v[14:17], v14 offset:3072
	ds_read_b128 v[18:21], v30
	ds_read_b128 v[22:25], v30 offset:1024
	ds_read_b128 v[26:29], v30 offset:2048
	ds_read_b128 v[30:33], v30 offset:3072
	s_add_u32 s10, s66, s28
	s_addc_u32 s11, s67, s29
	s_mov_b32 m0, s23
	v_lshl_add_u64 v[200:201], s[10:11], 0, v[162:163]
	ds_read_b128 v[184:187], v229 offset:32768
	ds_read_b128 v[188:191], v229 offset:33792
	ds_read_b128 v[192:195], v229 offset:34816
	ds_read_b128 v[196:199], v229 offset:35840
	ds_read_b128 v[210:213], v229 offset:36864
	ds_read_b128 v[214:217], v229 offset:37888
	ds_read_b128 v[218:221], v229 offset:38912
	ds_read_b128 v[222:225], v229 offset:39936
	global_load_lds_dwordx4 v[200:201], off
	v_lshl_add_u64 v[200:201], s[10:11], 0, v[164:165]
	s_mov_b32 m0, s26
	s_nop 0
	global_load_lds_dwordx4 v[200:201], off
	s_waitcnt vmcnt(8)
	s_waitcnt lgkmcnt(0)
	s_setprio 1
	s_barrier
	v_mfma_f32_16x16x128_f8f6f4 v[158:161], v[2:9], v[184:191], v[158:161]
	v_mfma_f32_16x16x128_f8f6f4 v[154:157], v[10:17], v[184:191], v[154:157]
	v_mfma_f32_16x16x128_f8f6f4 v[150:153], v[2:9], v[192:199], v[150:153]
	v_mfma_f32_16x16x128_f8f6f4 v[146:149], v[10:17], v[192:199], v[146:149]
	v_mfma_f32_16x16x128_f8f6f4 v[138:141], v[2:9], v[210:217], v[138:141]
	v_mfma_f32_16x16x128_f8f6f4 v[130:133], v[10:17], v[210:217], v[130:133]
	v_mfma_f32_16x16x128_f8f6f4 v[122:125], v[2:9], v[218:225], v[122:125]
	v_mfma_f32_16x16x128_f8f6f4 v[114:117], v[10:17], v[218:225], v[114:117]
	s_setprio 0
	s_setprio 1
	v_mfma_f32_16x16x128_f8f6f4 v[142:145], v[18:25], v[184:191], v[142:145]
	v_mfma_f32_16x16x128_f8f6f4 v[134:137], v[26:33], v[184:191], v[134:137]
	v_mfma_f32_16x16x128_f8f6f4 v[126:129], v[18:25], v[192:199], v[126:129]
	v_mfma_f32_16x16x128_f8f6f4 v[118:121], v[26:33], v[192:199], v[118:121]
	v_mfma_f32_16x16x128_f8f6f4 v[110:113], v[18:25], v[210:217], v[110:113]
	v_mfma_f32_16x16x128_f8f6f4 v[106:109], v[26:33], v[210:217], v[106:109]
	v_mfma_f32_16x16x128_f8f6f4 v[102:105], v[18:25], v[218:225], v[102:105]
	v_mfma_f32_16x16x128_f8f6f4 v[98:101], v[26:33], v[218:225], v[98:101]
	s_setprio 0
	s_barrier
	s_add_i32 s7, s7, s13
	v_lshl_add_u64 v[172:173], v[172:173], 0, s[14:15]
	s_mov_b32 m0, s7
	ds_read_b128 v[184:187], v229 offset:49152
	ds_read_b128 v[188:191], v229 offset:50176
	ds_read_b128 v[192:195], v229 offset:51200
	ds_read_b128 v[196:199], v229 offset:52224
	ds_read_b128 v[210:213], v229 offset:53248
	ds_read_b128 v[214:217], v229 offset:54272
	ds_read_b128 v[218:221], v229 offset:55296
	ds_read_b128 v[222:225], v229 offset:56320
	global_load_lds_dwordx4 v[172:173], off
	v_lshl_add_u64 v[172:173], v[174:175], 0, s[14:15]
	s_add_i32 m0, s7, 0x2000
	s_add_i32 s7, s68, s13
	global_load_lds_dwordx4 v[172:173], off
	v_lshl_add_u64 v[172:173], v[176:177], 0, s[14:15]
	s_mov_b32 m0, s7
	s_nop 0
	global_load_lds_dwordx4 v[172:173], off
	v_lshl_add_u64 v[172:173], v[178:179], 0, s[14:15]
	s_add_i32 m0, s7, 0x2000
	s_nop 0
	global_load_lds_dwordx4 v[172:173], off
	v_lshl_add_u64 v[172:173], v[180:181], 0, s[14:15]
	s_mov_b32 m0, s27
	s_nop 0
	global_load_lds_dwordx4 v[172:173], off
	v_lshl_add_u64 v[172:173], v[182:183], 0, s[14:15]
	s_mov_b32 m0, s70
	s_nop 0
	global_load_lds_dwordx4 v[172:173], off
	s_waitcnt vmcnt(8)
	s_waitcnt lgkmcnt(0)
	s_setprio 1
	s_barrier
	v_mfma_f32_16x16x128_f8f6f4 v[94:97], v[2:9], v[184:191], v[94:97]
	v_mfma_f32_16x16x128_f8f6f4 v[90:93], v[10:17], v[184:191], v[90:93]
	v_mfma_f32_16x16x128_f8f6f4 v[86:89], v[2:9], v[192:199], v[86:89]
	v_mfma_f32_16x16x128_f8f6f4 v[82:85], v[10:17], v[192:199], v[82:85]
	v_mfma_f32_16x16x128_f8f6f4 v[74:77], v[2:9], v[210:217], v[74:77]
	v_mfma_f32_16x16x128_f8f6f4 v[66:69], v[10:17], v[210:217], v[66:69]
	v_mfma_f32_16x16x128_f8f6f4 v[58:61], v[2:9], v[218:225], v[58:61]
	v_mfma_f32_16x16x128_f8f6f4 v[50:53], v[10:17], v[218:225], v[50:53]
	s_setprio 0
	s_setprio 1
	v_mfma_f32_16x16x128_f8f6f4 v[78:81], v[18:25], v[184:191], v[78:81]
	v_mfma_f32_16x16x128_f8f6f4 v[70:73], v[26:33], v[184:191], v[70:73]
	v_mfma_f32_16x16x128_f8f6f4 v[62:65], v[18:25], v[192:199], v[62:65]
	v_mfma_f32_16x16x128_f8f6f4 v[54:57], v[26:33], v[192:199], v[54:57]
	v_mfma_f32_16x16x128_f8f6f4 v[46:49], v[18:25], v[210:217], v[46:49]
	v_mfma_f32_16x16x128_f8f6f4 v[42:45], v[26:33], v[210:217], v[42:45]
	v_mfma_f32_16x16x128_f8f6f4 v[38:41], v[18:25], v[218:225], v[38:41]
	v_mfma_f32_16x16x128_f8f6f4 v[34:37], v[26:33], v[218:225], v[34:37]
	s_setprio 0
	s_barrier
	s_add_u32 s64, s64, 0x100
	s_addc_u32 s65, s65, 0
	s_add_u32 s97, s97, 0x100
	s_addc_u32 vcc_lo, vcc_lo, 0
	s_cmp_ge_i32 vcc_hi, s71
	s_mov_b32 s66, vcc_hi
	s_cbranch_scc0 .LBB0_1722
	v_pk_mul_f32 v[214:215], v[160:161], s[18:19] op_sel_hi:[1,0]
	v_pk_mul_f32 v[216:217], v[158:159], s[18:19] op_sel_hi:[1,0]
	v_pk_mul_f32 v[220:221], v[156:157], s[18:19] op_sel_hi:[1,0]
	v_pk_mul_f32 v[218:219], v[154:155], s[18:19] op_sel_hi:[1,0]
	v_pk_mul_f32 v[200:201], v[144:145], s[18:19] op_sel_hi:[1,0]
	v_pk_mul_f32 v[198:199], v[142:143], s[18:19] op_sel_hi:[1,0]
	v_pk_mul_f32 v[212:213], v[136:137], s[18:19] op_sel_hi:[1,0]
	v_pk_mul_f32 v[210:211], v[134:135], s[18:19] op_sel_hi:[1,0]
	v_pk_mul_f32 v[190:191], v[152:153], s[18:19] op_sel_hi:[1,0]
	v_pk_mul_f32 v[192:193], v[150:151], s[18:19] op_sel_hi:[1,0]
	v_pk_mul_f32 v[194:195], v[148:149], s[18:19] op_sel_hi:[1,0]
	v_pk_mul_f32 v[196:197], v[146:147], s[18:19] op_sel_hi:[1,0]
	v_pk_mul_f32 v[180:181], v[128:129], s[18:19] op_sel_hi:[1,0]
	v_pk_mul_f32 v[182:183], v[126:127], s[18:19] op_sel_hi:[1,0]
	v_pk_mul_f32 v[184:185], v[120:121], s[18:19] op_sel_hi:[1,0]
	v_pk_mul_f32 v[186:187], v[118:119], s[18:19] op_sel_hi:[1,0]
	v_pk_mul_f32 v[172:173], v[140:141], s[18:19] op_sel_hi:[1,0]
	v_pk_mul_f32 v[174:175], v[138:139], s[18:19] op_sel_hi:[1,0]
	v_pk_mul_f32 v[176:177], v[132:133], s[18:19] op_sel_hi:[1,0]
	v_pk_mul_f32 v[178:179], v[130:131], s[18:19] op_sel_hi:[1,0]
	v_pk_mul_f32 v[152:153], v[112:113], s[18:19] op_sel_hi:[1,0]
	v_pk_mul_f32 v[154:155], v[110:111], s[18:19] op_sel_hi:[1,0]
	v_pk_mul_f32 v[156:157], v[108:109], s[18:19] op_sel_hi:[1,0]
	v_pk_mul_f32 v[158:159], v[106:107], s[18:19] op_sel_hi:[1,0]
	v_pk_mul_f32 v[144:145], v[124:125], s[18:19] op_sel_hi:[1,0]
	v_pk_mul_f32 v[146:147], v[122:123], s[18:19] op_sel_hi:[1,0]
	v_pk_mul_f32 v[148:149], v[116:117], s[18:19] op_sel_hi:[1,0]
	v_pk_mul_f32 v[150:151], v[114:115], s[18:19] op_sel_hi:[1,0]
	v_pk_mul_f32 v[132:133], v[104:105], s[18:19] op_sel_hi:[1,0]
	v_pk_mul_f32 v[134:135], v[102:103], s[18:19] op_sel_hi:[1,0]
	v_pk_mul_f32 v[136:137], v[100:101], s[18:19] op_sel_hi:[1,0]
	v_pk_mul_f32 v[138:139], v[98:99], s[18:19] op_sel_hi:[1,0]
	v_pk_mul_f32 v[116:117], v[96:97], s[18:19] op_sel_hi:[1,0]
	v_pk_mul_f32 v[118:119], v[94:95], s[18:19] op_sel_hi:[1,0]
	v_pk_mul_f32 v[120:121], v[92:93], s[18:19] op_sel_hi:[1,0]
	v_pk_mul_f32 v[122:123], v[90:91], s[18:19] op_sel_hi:[1,0]
	v_pk_mul_f32 v[126:127], v[80:81], s[18:19] op_sel_hi:[1,0]
	v_pk_mul_f32 v[124:125], v[78:79], s[18:19] op_sel_hi:[1,0]
	v_pk_mul_f32 v[130:131], v[72:73], s[18:19] op_sel_hi:[1,0]
	v_pk_mul_f32 v[128:129], v[70:71], s[18:19] op_sel_hi:[1,0]
	v_pk_mul_f32 v[108:109], v[88:89], s[18:19] op_sel_hi:[1,0]
	v_pk_mul_f32 v[110:111], v[86:87], s[18:19] op_sel_hi:[1,0]
	v_pk_mul_f32 v[112:113], v[84:85], s[18:19] op_sel_hi:[1,0]
	v_pk_mul_f32 v[114:115], v[82:83], s[18:19] op_sel_hi:[1,0]
	v_pk_mul_f32 v[100:101], v[64:65], s[18:19] op_sel_hi:[1,0]
	v_pk_mul_f32 v[102:103], v[62:63], s[18:19] op_sel_hi:[1,0]
	v_pk_mul_f32 v[104:105], v[56:57], s[18:19] op_sel_hi:[1,0]
	v_pk_mul_f32 v[106:107], v[54:55], s[18:19] op_sel_hi:[1,0]
	v_pk_mul_f32 v[92:93], v[76:77], s[18:19] op_sel_hi:[1,0]
	v_pk_mul_f32 v[94:95], v[74:75], s[18:19] op_sel_hi:[1,0]
	v_pk_mul_f32 v[96:97], v[68:69], s[18:19] op_sel_hi:[1,0]
	v_pk_mul_f32 v[98:99], v[66:67], s[18:19] op_sel_hi:[1,0]
	v_pk_mul_f32 v[84:85], v[48:49], s[18:19] op_sel_hi:[1,0]
	v_pk_mul_f32 v[86:87], v[46:47], s[18:19] op_sel_hi:[1,0]
	v_pk_mul_f32 v[88:89], v[44:45], s[18:19] op_sel_hi:[1,0]
	v_pk_mul_f32 v[90:91], v[42:43], s[18:19] op_sel_hi:[1,0]
	v_pk_mul_f32 v[74:75], v[60:61], s[18:19] op_sel_hi:[1,0]
	v_pk_mul_f32 v[76:77], v[58:59], s[18:19] op_sel_hi:[1,0]
	v_pk_mul_f32 v[78:79], v[52:53], s[18:19] op_sel_hi:[1,0]
	v_pk_mul_f32 v[80:81], v[50:51], s[18:19] op_sel_hi:[1,0]
	v_pk_mul_f32 v[66:67], v[40:41], s[18:19] op_sel_hi:[1,0]
	v_pk_mul_f32 v[68:69], v[38:39], s[18:19] op_sel_hi:[1,0]
	v_pk_mul_f32 v[70:71], v[36:37], s[18:19] op_sel_hi:[1,0]
	v_pk_mul_f32 v[72:73], v[34:35], s[18:19] op_sel_hi:[1,0]

.LBB0_1774:
	s_add_i32 s78, s56, 2
	s_add_u32 s10, s54, 0x80
	s_addc_u32 s11, s55, 0
	s_add_i32 s7, 0, 0x10000
	s_cmp_eq_u32 s64, s56
	s_cselect_b32 s57, s39, s11
	s_cselect_b32 s56, s38, s10
	s_cselect_b32 s59, s53, s77
	s_cselect_b32 s58, s52, s75
	s_add_i32 s10, 0, 0x14000
	v_add_u32_e32 v2, s7, v190
	v_add_u32_e32 v6, s10, v190
	ds_read_b128 v[26:29], v2
	ds_read_b128 v[30:33], v2 offset:1024
	ds_read_b128 v[18:21], v2 offset:2048
	ds_read_b128 v[22:25], v2 offset:3072
	ds_read_b128 v[10:13], v6
	ds_read_b128 v[14:17], v6 offset:1024
	s_waitcnt lgkmcnt(0)
	ds_read_b128 v[2:5], v6 offset:2048
	ds_read_b128 v[6:9], v6 offset:3072
	v_lshl_add_u64 v[200:201], s[54:55], 0, v[168:169]
	s_add_i32 m0, s16, 0xc000
	ds_read_b128 v[172:175], v191
	ds_read_b128 v[176:179], v191 offset:1024
	ds_read_b128 v[180:183], v191 offset:2048
	ds_read_b128 v[184:187], v191 offset:3072
	ds_read_b128 v[192:195], v191 offset:4096
	ds_read_b128 v[196:199], v191 offset:5120
	ds_read_b128 v[210:213], v191 offset:6144
	ds_read_b128 v[214:217], v191 offset:7168
	global_load_lds_dwordx4 v[200:201], off
	v_lshl_add_u64 v[200:201], s[54:55], 0, v[170:171]
	s_add_i32 m0, s16, 0xe000
	s_nop 0
	global_load_lds_dwordx4 v[200:201], off
	s_waitcnt vmcnt(8)
	s_waitcnt lgkmcnt(0)
	s_setprio 1
	s_barrier
	v_mfma_f32_16x16x128_f8f6f4 v[158:161], v[26:33], v[172:179], v[158:161]
	v_mfma_f32_16x16x128_f8f6f4 v[154:157], v[18:25], v[172:179], v[154:157]
	v_mfma_f32_16x16x128_f8f6f4 v[150:153], v[26:33], v[180:187], v[150:153]
	v_mfma_f32_16x16x128_f8f6f4 v[146:149], v[18:25], v[180:187], v[146:149]
	v_mfma_f32_16x16x128_f8f6f4 v[138:141], v[26:33], v[192:199], v[138:141]
	v_mfma_f32_16x16x128_f8f6f4 v[130:133], v[18:25], v[192:199], v[130:133]
	v_mfma_f32_16x16x128_f8f6f4 v[122:125], v[26:33], v[210:217], v[122:125]
	v_mfma_f32_16x16x128_f8f6f4 v[114:117], v[18:25], v[210:217], v[114:117]
	s_setprio 0
	s_setprio 1
	v_mfma_f32_16x16x128_f8f6f4 v[142:145], v[10:17], v[172:179], v[142:145]
	v_mfma_f32_16x16x128_f8f6f4 v[134:137], v[2:9], v[172:179], v[134:137]
	v_mfma_f32_16x16x128_f8f6f4 v[126:129], v[10:17], v[180:187], v[126:129]
	v_mfma_f32_16x16x128_f8f6f4 v[118:121], v[2:9], v[180:187], v[118:121]
	v_mfma_f32_16x16x128_f8f6f4 v[110:113], v[10:17], v[192:199], v[110:113]
	v_mfma_f32_16x16x128_f8f6f4 v[106:109], v[2:9], v[192:199], v[106:109]
	v_mfma_f32_16x16x128_f8f6f4 v[102:105], v[10:17], v[210:217], v[102:105]
	v_mfma_f32_16x16x128_f8f6f4 v[98:101], v[2:9], v[210:217], v[98:101]
	s_setprio 0
	s_barrier
	s_add_i32 s7, s7, s13
	v_lshl_add_u64 v[172:173], s[58:59], 0, v[0:1]
	s_mov_b32 m0, s7
	ds_read_b128 v[192:195], v191 offset:16384
	ds_read_b128 v[196:199], v191 offset:17408
	ds_read_b128 v[210:213], v191 offset:18432
	ds_read_b128 v[214:217], v191 offset:19456
	ds_read_b128 v[218:221], v191 offset:20480
	ds_read_b128 v[222:225], v191 offset:21504
	ds_read_b128 v[246:249], v191 offset:22528
	ds_read_b128 v[250:253], v191 offset:23552
	global_load_lds_dwordx4 v[172:173], off
	s_add_i32 m0, s7, 0x2000
	v_lshl_add_u64 v[174:175], s[58:59], 0, v[166:167]
	s_add_u32 s58, s58, s28
	s_addc_u32 s59, s59, s29
	s_add_i32 s7, s10, s13
	global_load_lds_dwordx4 v[174:175], off
	v_lshl_add_u64 v[176:177], s[58:59], 0, v[0:1]
	s_mov_b32 m0, s7
	v_lshl_add_u64 v[178:179], s[58:59], 0, v[166:167]
	global_load_lds_dwordx4 v[176:177], off
	s_add_i32 m0, s7, 0x2000
	v_lshl_add_u64 v[180:181], s[56:57], 0, v[162:163]
	global_load_lds_dwordx4 v[178:179], off
	s_mov_b32 m0, s16
	v_lshl_add_u64 v[182:183], s[56:57], 0, v[164:165]
	global_load_lds_dwordx4 v[180:181], off
	s_mov_b32 m0, s17
	s_nop 0
	global_load_lds_dwordx4 v[182:183], off
	s_waitcnt vmcnt(8)
	s_waitcnt lgkmcnt(0)
	s_setprio 1
	s_barrier
	v_mfma_f32_16x16x128_f8f6f4 v[94:97], v[26:33], v[192:199], v[94:97]
	v_mfma_f32_16x16x128_f8f6f4 v[90:93], v[18:25], v[192:199], v[90:93]
	v_mfma_f32_16x16x128_f8f6f4 v[86:89], v[26:33], v[210:217], v[86:89]
	v_mfma_f32_16x16x128_f8f6f4 v[82:85], v[18:25], v[210:217], v[82:85]
	v_mfma_f32_16x16x128_f8f6f4 v[74:77], v[26:33], v[218:225], v[74:77]
	v_mfma_f32_16x16x128_f8f6f4 v[66:69], v[18:25], v[218:225], v[66:69]
	v_mfma_f32_16x16x128_f8f6f4 v[58:61], v[26:33], v[246:253], v[58:61]
	v_mfma_f32_16x16x128_f8f6f4 v[50:53], v[18:25], v[246:253], v[50:53]
	s_setprio 0
	s_setprio 1
	v_mfma_f32_16x16x128_f8f6f4 v[78:81], v[10:17], v[192:199], v[78:81]
	v_mfma_f32_16x16x128_f8f6f4 v[70:73], v[2:9], v[192:199], v[70:73]
	v_mfma_f32_16x16x128_f8f6f4 v[62:65], v[10:17], v[210:217], v[62:65]
	v_mfma_f32_16x16x128_f8f6f4 v[54:57], v[2:9], v[210:217], v[54:57]
	v_mfma_f32_16x16x128_f8f6f4 v[46:49], v[10:17], v[218:225], v[46:49]
	v_mfma_f32_16x16x128_f8f6f4 v[42:45], v[2:9], v[218:225], v[42:45]
	v_mfma_f32_16x16x128_f8f6f4 v[38:41], v[10:17], v[246:253], v[38:41]
	v_mfma_f32_16x16x128_f8f6f4 v[34:37], v[2:9], v[246:253], v[34:37]
	s_setprio 0
	s_barrier
	s_add_i32 s7, 0, 0x18000
	s_add_i32 s58, 0, 0x1c000
	v_add_u32_e32 v14, s7, v190
	v_add_u32_e32 v30, s58, v190
	ds_read_b128 v[2:5], v14
	ds_read_b128 v[6:9], v14 offset:1024
	ds_read_b128 v[10:13], v14 offset:2048
	ds_read_b128 v[14:17], v14 offset:3072
	ds_read_b128 v[18:21], v30
	ds_read_b128 v[22:25], v30 offset:1024
	ds_read_b128 v[26:29], v30 offset:2048
	ds_read_b128 v[30:33], v30 offset:3072
	s_add_u32 s10, s56, s28
	s_addc_u32 s11, s57, s29
	s_mov_b32 m0, s23
	v_lshl_add_u64 v[184:185], s[10:11], 0, v[162:163]
	ds_read_b128 v[192:195], v191 offset:32768
	ds_read_b128 v[196:199], v191 offset:33792
	ds_read_b128 v[210:213], v191 offset:34816
	ds_read_b128 v[214:217], v191 offset:35840
	ds_read_b128 v[218:221], v191 offset:36864
	ds_read_b128 v[222:225], v191 offset:37888
	ds_read_b128 v[246:249], v191 offset:38912
	ds_read_b128 v[250:253], v191 offset:39936
	global_load_lds_dwordx4 v[184:185], off
	v_lshl_add_u64 v[184:185], s[10:11], 0, v[164:165]
	s_mov_b32 m0, s26
	s_nop 0
	global_load_lds_dwordx4 v[184:185], off
	s_waitcnt vmcnt(8)
	s_waitcnt lgkmcnt(0)
	s_setprio 1
	s_barrier
	v_mfma_f32_16x16x128_f8f6f4 v[158:161], v[2:9], v[192:199], v[158:161]
	v_mfma_f32_16x16x128_f8f6f4 v[154:157], v[10:17], v[192:199], v[154:157]
	v_mfma_f32_16x16x128_f8f6f4 v[150:153], v[2:9], v[210:217], v[150:153]
	v_mfma_f32_16x16x128_f8f6f4 v[146:149], v[10:17], v[210:217], v[146:149]
	v_mfma_f32_16x16x128_f8f6f4 v[138:141], v[2:9], v[218:225], v[138:141]
	v_mfma_f32_16x16x128_f8f6f4 v[130:133], v[10:17], v[218:225], v[130:133]
	v_mfma_f32_16x16x128_f8f6f4 v[122:125], v[2:9], v[246:253], v[122:125]
	v_mfma_f32_16x16x128_f8f6f4 v[114:117], v[10:17], v[246:253], v[114:117]
	s_setprio 0
	s_setprio 1
	v_mfma_f32_16x16x128_f8f6f4 v[142:145], v[18:25], v[192:199], v[142:145]
	v_mfma_f32_16x16x128_f8f6f4 v[134:137], v[26:33], v[192:199], v[134:137]
	v_mfma_f32_16x16x128_f8f6f4 v[126:129], v[18:25], v[210:217], v[126:129]
	v_mfma_f32_16x16x128_f8f6f4 v[118:121], v[26:33], v[210:217], v[118:121]
	v_mfma_f32_16x16x128_f8f6f4 v[110:113], v[18:25], v[218:225], v[110:113]
	v_mfma_f32_16x16x128_f8f6f4 v[106:109], v[26:33], v[218:225], v[106:109]
	v_mfma_f32_16x16x128_f8f6f4 v[102:105], v[18:25], v[246:253], v[102:105]
	v_mfma_f32_16x16x128_f8f6f4 v[98:101], v[26:33], v[246:253], v[98:101]
	s_setprio 0
	s_barrier
	s_add_i32 s7, s7, s13
	v_lshl_add_u64 v[172:173], v[172:173], 0, s[14:15]
	s_mov_b32 m0, s7
	ds_read_b128 v[192:195], v191 offset:49152
	ds_read_b128 v[196:199], v191 offset:50176
	ds_read_b128 v[210:213], v191 offset:51200
	ds_read_b128 v[214:217], v191 offset:52224
	ds_read_b128 v[218:221], v191 offset:53248
	ds_read_b128 v[222:225], v191 offset:54272
	ds_read_b128 v[246:249], v191 offset:55296
	ds_read_b128 v[250:253], v191 offset:56320
	global_load_lds_dwordx4 v[172:173], off
	v_lshl_add_u64 v[172:173], v[174:175], 0, s[14:15]
	s_add_i32 m0, s7, 0x2000
	s_add_i32 s7, s58, s13
	global_load_lds_dwordx4 v[172:173], off
	v_lshl_add_u64 v[172:173], v[176:177], 0, s[14:15]
	s_mov_b32 m0, s7
	s_nop 0
	global_load_lds_dwordx4 v[172:173], off
	v_lshl_add_u64 v[172:173], v[178:179], 0, s[14:15]
	s_add_i32 m0, s7, 0x2000
	s_nop 0
	global_load_lds_dwordx4 v[172:173], off
	v_lshl_add_u64 v[172:173], v[180:181], 0, s[14:15]
	s_mov_b32 m0, s27
	s_nop 0
	global_load_lds_dwordx4 v[172:173], off
	v_lshl_add_u64 v[172:173], v[182:183], 0, s[14:15]
	s_mov_b32 m0, s60
	s_nop 0
	global_load_lds_dwordx4 v[172:173], off
	s_waitcnt vmcnt(8)
	s_waitcnt lgkmcnt(0)
	s_setprio 1
	s_barrier
	v_mfma_f32_16x16x128_f8f6f4 v[94:97], v[2:9], v[192:199], v[94:97]
	v_mfma_f32_16x16x128_f8f6f4 v[90:93], v[10:17], v[192:199], v[90:93]
	v_mfma_f32_16x16x128_f8f6f4 v[86:89], v[2:9], v[210:217], v[86:89]
	v_mfma_f32_16x16x128_f8f6f4 v[82:85], v[10:17], v[210:217], v[82:85]
	v_mfma_f32_16x16x128_f8f6f4 v[74:77], v[2:9], v[218:225], v[74:77]
	v_mfma_f32_16x16x128_f8f6f4 v[66:69], v[10:17], v[218:225], v[66:69]
	v_mfma_f32_16x16x128_f8f6f4 v[58:61], v[2:9], v[246:253], v[58:61]
	v_mfma_f32_16x16x128_f8f6f4 v[50:53], v[10:17], v[246:253], v[50:53]
	s_setprio 0
	s_setprio 1
	v_mfma_f32_16x16x128_f8f6f4 v[78:81], v[18:25], v[192:199], v[78:81]
	v_mfma_f32_16x16x128_f8f6f4 v[70:73], v[26:33], v[192:199], v[70:73]
	v_mfma_f32_16x16x128_f8f6f4 v[62:65], v[18:25], v[210:217], v[62:65]
	v_mfma_f32_16x16x128_f8f6f4 v[54:57], v[26:33], v[210:217], v[54:57]
	v_mfma_f32_16x16x128_f8f6f4 v[46:49], v[18:25], v[218:225], v[46:49]
	v_mfma_f32_16x16x128_f8f6f4 v[42:45], v[26:33], v[218:225], v[42:45]
	v_mfma_f32_16x16x128_f8f6f4 v[38:41], v[18:25], v[246:253], v[38:41]
	v_mfma_f32_16x16x128_f8f6f4 v[34:37], v[26:33], v[246:253], v[34:37]
	s_setprio 0
	s_barrier
	s_add_u32 s54, s54, 0x100
	s_addc_u32 s55, s55, 0
	s_add_u32 s75, s75, 0x100
	s_addc_u32 s77, s77, 0
	s_cmp_ge_i32 s78, s61
	s_mov_b32 s56, s78
	s_cbranch_scc0 .LBB0_1774
	v_pk_mul_f32 v[160:161], v[160:161], s[18:19] op_sel_hi:[1,0]
	v_pk_mul_f32 v[158:159], v[158:159], s[18:19] op_sel_hi:[1,0]
	v_pk_mul_f32 v[172:173], v[156:157], s[18:19] op_sel_hi:[1,0]
	v_pk_mul_f32 v[174:175], v[154:155], s[18:19] op_sel_hi:[1,0]
	v_pk_mul_f32 v[176:177], v[144:145], s[18:19] op_sel_hi:[1,0]
	v_pk_mul_f32 v[178:179], v[142:143], s[18:19] op_sel_hi:[1,0]
	v_pk_mul_f32 v[180:181], v[136:137], s[18:19] op_sel_hi:[1,0]
	v_pk_mul_f32 v[182:183], v[134:135], s[18:19] op_sel_hi:[1,0]
	v_pk_mul_f32 v[156:157], v[152:153], s[18:19] op_sel_hi:[1,0]
	v_pk_mul_f32 v[154:155], v[150:151], s[18:19] op_sel_hi:[1,0]
	v_pk_mul_f32 v[152:153], v[148:149], s[18:19] op_sel_hi:[1,0]
	v_pk_mul_f32 v[150:151], v[146:147], s[18:19] op_sel_hi:[1,0]
	v_pk_mul_f32 v[148:149], v[128:129], s[18:19] op_sel_hi:[1,0]
	v_pk_mul_f32 v[146:147], v[126:127], s[18:19] op_sel_hi:[1,0]
	v_pk_mul_f32 v[144:145], v[120:121], s[18:19] op_sel_hi:[1,0]
	v_pk_mul_f32 v[142:143], v[118:119], s[18:19] op_sel_hi:[1,0]
	v_pk_mul_f32 v[126:127], v[140:141], s[18:19] op_sel_hi:[1,0]
	v_pk_mul_f32 v[128:129], v[138:139], s[18:19] op_sel_hi:[1,0]
	v_pk_mul_f32 v[132:133], v[132:133], s[18:19] op_sel_hi:[1,0]
	v_pk_mul_f32 v[130:131], v[130:131], s[18:19] op_sel_hi:[1,0]
	v_pk_mul_f32 v[134:135], v[112:113], s[18:19] op_sel_hi:[1,0]
	v_pk_mul_f32 v[136:137], v[110:111], s[18:19] op_sel_hi:[1,0]
	v_pk_mul_f32 v[138:139], v[108:109], s[18:19] op_sel_hi:[1,0]
	v_pk_mul_f32 v[140:141], v[106:107], s[18:19] op_sel_hi:[1,0]
	v_pk_mul_f32 v[120:121], v[124:125], s[18:19] op_sel_hi:[1,0]
	v_pk_mul_f32 v[118:119], v[122:123], s[18:19] op_sel_hi:[1,0]
	v_pk_mul_f32 v[116:117], v[116:117], s[18:19] op_sel_hi:[1,0]
	v_pk_mul_f32 v[114:115], v[114:115], s[18:19] op_sel_hi:[1,0]
	v_pk_mul_f32 v[112:113], v[104:105], s[18:19] op_sel_hi:[1,0]
	v_pk_mul_f32 v[110:111], v[102:103], s[18:19] op_sel_hi:[1,0]
	v_pk_mul_f32 v[108:109], v[100:101], s[18:19] op_sel_hi:[1,0]
	v_pk_mul_f32 v[106:107], v[98:99], s[18:19] op_sel_hi:[1,0]
	v_pk_mul_f32 v[96:97], v[96:97], s[18:19] op_sel_hi:[1,0]
	v_pk_mul_f32 v[94:95], v[94:95], s[18:19] op_sel_hi:[1,0]
	v_pk_mul_f32 v[92:93], v[92:93], s[18:19] op_sel_hi:[1,0]
	v_pk_mul_f32 v[90:91], v[90:91], s[18:19] op_sel_hi:[1,0]
	v_pk_mul_f32 v[98:99], v[80:81], s[18:19] op_sel_hi:[1,0]
	v_pk_mul_f32 v[100:101], v[78:79], s[18:19] op_sel_hi:[1,0]
	v_pk_mul_f32 v[102:103], v[72:73], s[18:19] op_sel_hi:[1,0]
	v_pk_mul_f32 v[104:105], v[70:71], s[18:19] op_sel_hi:[1,0]
	v_pk_mul_f32 v[88:89], v[88:89], s[18:19] op_sel_hi:[1,0]
	v_pk_mul_f32 v[86:87], v[86:87], s[18:19] op_sel_hi:[1,0]
	v_pk_mul_f32 v[84:85], v[84:85], s[18:19] op_sel_hi:[1,0]
	v_pk_mul_f32 v[82:83], v[82:83], s[18:19] op_sel_hi:[1,0]
	v_pk_mul_f32 v[80:81], v[64:65], s[18:19] op_sel_hi:[1,0]
	v_pk_mul_f32 v[78:79], v[62:63], s[18:19] op_sel_hi:[1,0]
	v_pk_mul_f32 v[72:73], v[56:57], s[18:19] op_sel_hi:[1,0]
	v_pk_mul_f32 v[70:71], v[54:55], s[18:19] op_sel_hi:[1,0]
	v_pk_mul_f32 v[54:55], v[76:77], s[18:19] op_sel_hi:[1,0]
	v_pk_mul_f32 v[56:57], v[74:75], s[18:19] op_sel_hi:[1,0]
	v_pk_mul_f32 v[62:63], v[68:69], s[18:19] op_sel_hi:[1,0]
	v_pk_mul_f32 v[64:65], v[66:67], s[18:19] op_sel_hi:[1,0]
	v_pk_mul_f32 v[48:49], v[48:49], s[18:19] op_sel_hi:[1,0]
	v_pk_mul_f32 v[46:47], v[46:47], s[18:19] op_sel_hi:[1,0]
	v_pk_mul_f32 v[44:45], v[44:45], s[18:19] op_sel_hi:[1,0]
	v_pk_mul_f32 v[42:43], v[42:43], s[18:19] op_sel_hi:[1,0]
	v_pk_mul_f32 v[32:33], v[60:61], s[18:19] op_sel_hi:[1,0]
	v_pk_mul_f32 v[30:31], v[58:59], s[18:19] op_sel_hi:[1,0]
	v_pk_mul_f32 v[28:29], v[52:53], s[18:19] op_sel_hi:[1,0]
	v_pk_mul_f32 v[26:27], v[50:51], s[18:19] op_sel_hi:[1,0]
	v_pk_mul_f32 v[24:25], v[40:41], s[18:19] op_sel_hi:[1,0]
	v_pk_mul_f32 v[22:23], v[38:39], s[18:19] op_sel_hi:[1,0]
	v_pk_mul_f32 v[20:21], v[36:37], s[18:19] op_sel_hi:[1,0]
	v_pk_mul_f32 v[18:19], v[34:35], s[18:19] op_sel_hi:[1,0]

.LBB0_1873:
	s_add_i32 s69, s54, 2
	s_add_u32 s7, s52, 0x80
	s_addc_u32 s10, s53, 0
	s_add_i32 s70, 0, 0x10000
	s_cmp_eq_u32 s61, s54
	s_cselect_b32 s55, s39, s10
	s_cselect_b32 s54, s38, s7
	s_cselect_b32 s11, s51, s68
	s_cselect_b32 s10, s50, s67
	s_add_i32 s7, 0, 0x14000
	v_add_u32_e32 v46, s70, v178
	v_add_u32_e32 v62, s7, v178
	ds_read_b128 v[34:37], v46
	ds_read_b128 v[38:41], v46 offset:1024
	ds_read_b128 v[42:45], v46 offset:2048
	ds_read_b128 v[46:49], v46 offset:3072
	ds_read_b128 v[50:53], v62
	ds_read_b128 v[54:57], v62 offset:1024
	ds_read_b128 v[58:61], v62 offset:2048
	ds_read_b128 v[62:65], v62 offset:3072
	v_lshl_add_u64 v[200:201], s[52:53], 0, v[168:169]
	s_add_i32 m0, s23, 0xc000
	ds_read_b128 v[172:175], v179
	ds_read_b128 v[180:183], v179 offset:1024
	ds_read_b128 v[184:187], v179 offset:2048
	ds_read_b128 v[188:191], v179 offset:3072
	ds_read_b128 v[192:195], v179 offset:4096
	ds_read_b128 v[196:199], v179 offset:5120
	ds_read_b128 v[210:213], v179 offset:6144
	ds_read_b128 v[214:217], v179 offset:7168
	global_load_lds_dwordx4 v[200:201], off
	v_lshl_add_u64 v[200:201], s[52:53], 0, v[170:171]
	s_add_i32 m0, s23, 0xe000
	s_nop 0
	global_load_lds_dwordx4 v[200:201], off
	s_waitcnt vmcnt(8)
	s_waitcnt lgkmcnt(0)
	s_setprio 1
	s_barrier
	v_mfma_f32_16x16x32_bf16 v[158:161], v[34:37], v[172:175], v[158:161]
	v_mfma_f32_16x16x32_bf16 v[154:157], v[42:45], v[172:175], v[154:157]
	v_mfma_f32_16x16x32_bf16 v[142:145], v[34:37], v[184:187], v[142:145]
	v_mfma_f32_16x16x32_bf16 v[138:141], v[42:45], v[184:187], v[138:141]
	v_mfma_f32_16x16x32_bf16 v[126:129], v[34:37], v[192:195], v[126:129]
	v_mfma_f32_16x16x32_bf16 v[122:125], v[42:45], v[192:195], v[122:125]
	v_mfma_f32_16x16x32_bf16 v[110:113], v[34:37], v[210:213], v[110:113]
	v_mfma_f32_16x16x32_bf16 v[106:109], v[42:45], v[210:213], v[106:109]
	v_mfma_f32_16x16x32_bf16 v[158:161], v[38:41], v[180:183], v[158:161]
	v_mfma_f32_16x16x32_bf16 v[154:157], v[46:49], v[180:183], v[154:157]
	v_mfma_f32_16x16x32_bf16 v[142:145], v[38:41], v[188:191], v[142:145]
	v_mfma_f32_16x16x32_bf16 v[138:141], v[46:49], v[188:191], v[138:141]
	v_mfma_f32_16x16x32_bf16 v[126:129], v[38:41], v[196:199], v[126:129]
	v_mfma_f32_16x16x32_bf16 v[122:125], v[46:49], v[196:199], v[122:125]
	v_mfma_f32_16x16x32_bf16 v[110:113], v[38:41], v[214:217], v[110:113]
	v_mfma_f32_16x16x32_bf16 v[106:109], v[46:49], v[214:217], v[106:109]
	s_setprio 0
	s_setprio 1
	v_mfma_f32_16x16x32_bf16 v[150:153], v[50:53], v[172:175], v[150:153]
	v_mfma_f32_16x16x32_bf16 v[146:149], v[58:61], v[172:175], v[146:149]
	v_mfma_f32_16x16x32_bf16 v[134:137], v[50:53], v[184:187], v[134:137]
	v_mfma_f32_16x16x32_bf16 v[130:133], v[58:61], v[184:187], v[130:133]
	v_mfma_f32_16x16x32_bf16 v[118:121], v[50:53], v[192:195], v[118:121]
	v_mfma_f32_16x16x32_bf16 v[114:117], v[58:61], v[192:195], v[114:117]
	v_mfma_f32_16x16x32_bf16 v[102:105], v[50:53], v[210:213], v[102:105]
	v_mfma_f32_16x16x32_bf16 v[98:101], v[58:61], v[210:213], v[98:101]
	v_mfma_f32_16x16x32_bf16 v[150:153], v[54:57], v[180:183], v[150:153]
	v_mfma_f32_16x16x32_bf16 v[146:149], v[62:65], v[180:183], v[146:149]
	v_mfma_f32_16x16x32_bf16 v[134:137], v[54:57], v[188:191], v[134:137]
	v_mfma_f32_16x16x32_bf16 v[130:133], v[62:65], v[188:191], v[130:133]
	v_mfma_f32_16x16x32_bf16 v[118:121], v[54:57], v[196:199], v[118:121]
	v_mfma_f32_16x16x32_bf16 v[114:117], v[62:65], v[196:199], v[114:117]
	v_mfma_f32_16x16x32_bf16 v[102:105], v[54:57], v[214:217], v[102:105]
	v_mfma_f32_16x16x32_bf16 v[98:101], v[62:65], v[214:217], v[98:101]
	s_setprio 0
	s_barrier
	s_add_i32 s70, s70, s17
	v_lshl_add_u64 v[200:201], s[10:11], 0, v[0:1]
	s_mov_b32 m0, s70
	ds_read_b128 v[172:175], v179 offset:16384
	ds_read_b128 v[180:183], v179 offset:17408
	ds_read_b128 v[184:187], v179 offset:18432
	ds_read_b128 v[188:191], v179 offset:19456
	ds_read_b128 v[192:195], v179 offset:20480
	ds_read_b128 v[196:199], v179 offset:21504
	ds_read_b128 v[210:213], v179 offset:22528
	ds_read_b128 v[214:217], v179 offset:23552
	global_load_lds_dwordx4 v[200:201], off
	s_add_i32 m0, s70, 0x2000
	v_lshl_add_u64 v[202:203], s[10:11], 0, v[166:167]
	s_add_u32 s10, s10, s0
	s_addc_u32 s11, s11, s1
	s_add_i32 s7, s7, s17
	global_load_lds_dwordx4 v[202:203], off
	v_lshl_add_u64 v[226:227], s[10:11], 0, v[0:1]
	s_mov_b32 m0, s7
	v_lshl_add_u64 v[228:229], s[10:11], 0, v[166:167]
	global_load_lds_dwordx4 v[226:227], off
	s_add_i32 m0, s7, 0x2000
	v_lshl_add_u64 v[230:231], s[54:55], 0, v[162:163]
	global_load_lds_dwordx4 v[228:229], off
	s_mov_b32 m0, s23
	v_lshl_add_u64 v[232:233], s[54:55], 0, v[164:165]
	global_load_lds_dwordx4 v[230:231], off
	s_mov_b32 m0, s26
	s_nop 0
	global_load_lds_dwordx4 v[232:233], off
	s_waitcnt vmcnt(8)
	s_waitcnt lgkmcnt(0)
	s_setprio 1
	s_barrier
	v_mfma_f32_16x16x32_bf16 v[94:97], v[34:37], v[172:175], v[94:97]
	v_mfma_f32_16x16x32_bf16 v[90:93], v[42:45], v[172:175], v[90:93]
	v_mfma_f32_16x16x32_bf16 v[78:81], v[34:37], v[184:187], v[78:81]
	v_mfma_f32_16x16x32_bf16 v[74:77], v[42:45], v[184:187], v[74:77]
	v_mfma_f32_16x16x32_bf16 v[30:33], v[34:37], v[192:195], v[30:33]
	v_mfma_f32_16x16x32_bf16 v[26:29], v[42:45], v[192:195], v[26:29]
	v_mfma_f32_16x16x32_bf16 v[14:17], v[34:37], v[210:213], v[14:17]
	v_mfma_f32_16x16x32_bf16 v[10:13], v[42:45], v[210:213], v[10:13]
	v_mfma_f32_16x16x32_bf16 v[94:97], v[38:41], v[180:183], v[94:97]
	v_mfma_f32_16x16x32_bf16 v[90:93], v[46:49], v[180:183], v[90:93]
	v_mfma_f32_16x16x32_bf16 v[78:81], v[38:41], v[188:191], v[78:81]
	v_mfma_f32_16x16x32_bf16 v[74:77], v[46:49], v[188:191], v[74:77]
	v_mfma_f32_16x16x32_bf16 v[30:33], v[38:41], v[196:199], v[30:33]
	v_mfma_f32_16x16x32_bf16 v[26:29], v[46:49], v[196:199], v[26:29]
	v_mfma_f32_16x16x32_bf16 v[14:17], v[38:41], v[214:217], v[14:17]
	v_mfma_f32_16x16x32_bf16 v[10:13], v[46:49], v[214:217], v[10:13]
	s_setprio 0
	s_setprio 1
	v_mfma_f32_16x16x32_bf16 v[22:25], v[50:53], v[192:195], v[22:25]
	v_mfma_f32_16x16x32_bf16 v[18:21], v[58:61], v[192:195], v[18:21]
	v_mfma_f32_16x16x32_bf16 v[6:9], v[50:53], v[210:213], v[6:9]
	v_mfma_f32_16x16x32_bf16 v[2:5], v[58:61], v[210:213], v[2:5]
	v_mfma_f32_16x16x32_bf16 v[34:37], v[50:53], v[172:175], v[86:89]
	v_mfma_f32_16x16x32_bf16 v[38:41], v[58:61], v[172:175], v[82:85]
	v_mfma_f32_16x16x32_bf16 v[42:45], v[50:53], v[184:187], v[70:73]
	v_mfma_f32_16x16x32_bf16 v[46:49], v[58:61], v[184:187], v[66:69]
	v_mfma_f32_16x16x32_bf16 v[22:25], v[54:57], v[196:199], v[22:25]
	v_mfma_f32_16x16x32_bf16 v[18:21], v[62:65], v[196:199], v[18:21]
	v_mfma_f32_16x16x32_bf16 v[6:9], v[54:57], v[214:217], v[6:9]
	v_mfma_f32_16x16x32_bf16 v[2:5], v[62:65], v[214:217], v[2:5]
	v_mfma_f32_16x16x32_bf16 v[34:37], v[54:57], v[180:183], v[34:37]
	v_mfma_f32_16x16x32_bf16 v[38:41], v[62:65], v[180:183], v[38:41]
	v_mfma_f32_16x16x32_bf16 v[42:45], v[54:57], v[188:191], v[42:45]
	v_mfma_f32_16x16x32_bf16 v[46:49], v[62:65], v[188:191], v[46:49]
	s_setprio 0
	s_barrier
	s_add_i32 s7, 0, 0x18000
	s_add_i32 s70, 0, 0x1c000
	v_add_u32_e32 v62, s7, v178
	v_add_u32_e32 v66, s70, v178
	ds_read_b128 v[50:53], v62
	ds_read_b128 v[54:57], v62 offset:1024
	ds_read_b128 v[58:61], v62 offset:2048
	ds_read_b128 v[62:65], v62 offset:3072
	ds_read_b128 v[172:175], v66
	ds_read_b128 v[180:183], v66 offset:1024
	ds_read_b128 v[184:187], v66 offset:2048
	ds_read_b128 v[188:191], v66 offset:3072
	s_add_u32 s10, s54, s0
	s_addc_u32 s11, s55, s1
	s_mov_b32 m0, s27
	v_lshl_add_u64 v[218:219], s[10:11], 0, v[162:163]
	ds_read_b128 v[66:69], v179 offset:32768
	ds_read_b128 v[70:73], v179 offset:33792
	ds_read_b128 v[82:85], v179 offset:34816
	ds_read_b128 v[86:89], v179 offset:35840
	ds_read_b128 v[192:195], v179 offset:36864
	ds_read_b128 v[196:199], v179 offset:37888
	ds_read_b128 v[210:213], v179 offset:38912
	ds_read_b128 v[214:217], v179 offset:39936
	global_load_lds_dwordx4 v[218:219], off
	v_lshl_add_u64 v[218:219], s[10:11], 0, v[164:165]
	s_mov_b32 m0, s56
	s_nop 0
	global_load_lds_dwordx4 v[218:219], off
	s_waitcnt vmcnt(8)
	s_waitcnt lgkmcnt(0)
	s_setprio 1
	s_barrier
	v_mfma_f32_16x16x32_bf16 v[158:161], v[50:53], v[66:69], v[158:161]
	v_mfma_f32_16x16x32_bf16 v[154:157], v[58:61], v[66:69], v[154:157]
	v_mfma_f32_16x16x32_bf16 v[142:145], v[50:53], v[82:85], v[142:145]
	v_mfma_f32_16x16x32_bf16 v[138:141], v[58:61], v[82:85], v[138:141]
	v_mfma_f32_16x16x32_bf16 v[126:129], v[50:53], v[192:195], v[126:129]
	v_mfma_f32_16x16x32_bf16 v[122:125], v[58:61], v[192:195], v[122:125]
	v_mfma_f32_16x16x32_bf16 v[110:113], v[50:53], v[210:213], v[110:113]
	v_mfma_f32_16x16x32_bf16 v[106:109], v[58:61], v[210:213], v[106:109]
	v_mfma_f32_16x16x32_bf16 v[158:161], v[54:57], v[70:73], v[158:161]
	v_mfma_f32_16x16x32_bf16 v[154:157], v[62:65], v[70:73], v[154:157]
	v_mfma_f32_16x16x32_bf16 v[142:145], v[54:57], v[86:89], v[142:145]
	v_mfma_f32_16x16x32_bf16 v[138:141], v[62:65], v[86:89], v[138:141]
	v_mfma_f32_16x16x32_bf16 v[126:129], v[54:57], v[196:199], v[126:129]
	v_mfma_f32_16x16x32_bf16 v[122:125], v[62:65], v[196:199], v[122:125]
	v_mfma_f32_16x16x32_bf16 v[110:113], v[54:57], v[214:217], v[110:113]
	v_mfma_f32_16x16x32_bf16 v[106:109], v[62:65], v[214:217], v[106:109]
	s_setprio 0
	s_setprio 1
	v_mfma_f32_16x16x32_bf16 v[150:153], v[172:175], v[66:69], v[150:153]
	v_mfma_f32_16x16x32_bf16 v[66:69], v[184:187], v[66:69], v[146:149]
	v_mfma_f32_16x16x32_bf16 v[146:149], v[188:191], v[70:73], v[66:69]
	v_mfma_f32_16x16x32_bf16 v[66:69], v[172:175], v[82:85], v[134:137]
	v_mfma_f32_16x16x32_bf16 v[134:137], v[180:183], v[86:89], v[66:69]
	v_mfma_f32_16x16x32_bf16 v[66:69], v[184:187], v[82:85], v[130:133]
	v_mfma_f32_16x16x32_bf16 v[130:133], v[188:191], v[86:89], v[66:69]
	v_mfma_f32_16x16x32_bf16 v[66:69], v[172:175], v[192:195], v[118:121]
	v_mfma_f32_16x16x32_bf16 v[118:121], v[180:183], v[196:199], v[66:69]
	v_mfma_f32_16x16x32_bf16 v[66:69], v[184:187], v[192:195], v[114:117]
	v_mfma_f32_16x16x32_bf16 v[114:117], v[188:191], v[196:199], v[66:69]
	v_mfma_f32_16x16x32_bf16 v[66:69], v[172:175], v[210:213], v[102:105]
	v_mfma_f32_16x16x32_bf16 v[102:105], v[180:183], v[214:217], v[66:69]
	v_mfma_f32_16x16x32_bf16 v[66:69], v[184:187], v[210:213], v[98:101]
	v_mfma_f32_16x16x32_bf16 v[150:153], v[180:183], v[70:73], v[150:153]
	v_mfma_f32_16x16x32_bf16 v[98:101], v[188:191], v[214:217], v[66:69]
	s_setprio 0
	s_barrier
	s_add_i32 s7, s7, s17
	v_lshl_add_u64 v[82:83], v[200:201], 0, s[14:15]
	s_mov_b32 m0, s7
	s_nop 0
	ds_read_b128 v[66:69], v179 offset:49152
	ds_read_b128 v[70:73], v179 offset:50176
	ds_read_b128 v[192:195], v179 offset:51200
	ds_read_b128 v[196:199], v179 offset:52224
	ds_read_b128 v[210:213], v179 offset:53248
	ds_read_b128 v[214:217], v179 offset:54272
	ds_read_b128 v[218:221], v179 offset:55296
	ds_read_b128 v[222:225], v179 offset:56320
	global_load_lds_dwordx4 v[82:83], off
	v_lshl_add_u64 v[82:83], v[202:203], 0, s[14:15]
	s_add_i32 m0, s7, 0x2000
	s_add_i32 s7, s70, s17
	global_load_lds_dwordx4 v[82:83], off
	v_lshl_add_u64 v[82:83], v[226:227], 0, s[14:15]
	s_mov_b32 m0, s7
	s_nop 0
	global_load_lds_dwordx4 v[82:83], off
	v_lshl_add_u64 v[82:83], v[228:229], 0, s[14:15]
	s_add_i32 m0, s7, 0x2000
	s_nop 0
	global_load_lds_dwordx4 v[82:83], off
	v_lshl_add_u64 v[82:83], v[230:231], 0, s[14:15]
	s_mov_b32 m0, s8
	s_nop 0
	global_load_lds_dwordx4 v[82:83], off
	v_lshl_add_u64 v[82:83], v[232:233], 0, s[14:15]
	s_mov_b32 m0, s57
	s_nop 0
	global_load_lds_dwordx4 v[82:83], off
	s_waitcnt vmcnt(8)
	s_waitcnt lgkmcnt(0)
	s_setprio 1
	s_barrier
	v_mfma_f32_16x16x32_bf16 v[82:85], v[50:53], v[66:69], v[94:97]
	v_mfma_f32_16x16x32_bf16 v[94:97], v[54:57], v[70:73], v[82:85]
	v_mfma_f32_16x16x32_bf16 v[82:85], v[58:61], v[66:69], v[90:93]
	v_mfma_f32_16x16x32_bf16 v[78:81], v[50:53], v[192:195], v[78:81]
	v_mfma_f32_16x16x32_bf16 v[74:77], v[58:61], v[192:195], v[74:77]
	v_mfma_f32_16x16x32_bf16 v[30:33], v[50:53], v[210:213], v[30:33]
	v_mfma_f32_16x16x32_bf16 v[26:29], v[58:61], v[210:213], v[26:29]
	v_mfma_f32_16x16x32_bf16 v[14:17], v[50:53], v[218:221], v[14:17]
	v_mfma_f32_16x16x32_bf16 v[10:13], v[58:61], v[218:221], v[10:13]
	v_mfma_f32_16x16x32_bf16 v[90:93], v[62:65], v[70:73], v[82:85]
	v_mfma_f32_16x16x32_bf16 v[78:81], v[54:57], v[196:199], v[78:81]
	v_mfma_f32_16x16x32_bf16 v[74:77], v[62:65], v[196:199], v[74:77]
	v_mfma_f32_16x16x32_bf16 v[30:33], v[54:57], v[214:217], v[30:33]
	v_mfma_f32_16x16x32_bf16 v[26:29], v[62:65], v[214:217], v[26:29]
	v_mfma_f32_16x16x32_bf16 v[14:17], v[54:57], v[222:225], v[14:17]
	v_mfma_f32_16x16x32_bf16 v[10:13], v[62:65], v[222:225], v[10:13]
	s_setprio 0
	s_setprio 1
	v_mfma_f32_16x16x32_bf16 v[34:37], v[172:175], v[66:69], v[34:37]
	v_mfma_f32_16x16x32_bf16 v[86:89], v[180:183], v[70:73], v[34:37]
	v_mfma_f32_16x16x32_bf16 v[34:37], v[184:187], v[66:69], v[38:41]
	v_mfma_f32_16x16x32_bf16 v[82:85], v[188:191], v[70:73], v[34:37]
	v_mfma_f32_16x16x32_bf16 v[34:37], v[172:175], v[192:195], v[42:45]
	v_mfma_f32_16x16x32_bf16 v[70:73], v[180:183], v[196:199], v[34:37]
	v_mfma_f32_16x16x32_bf16 v[34:37], v[184:187], v[192:195], v[46:49]
	v_mfma_f32_16x16x32_bf16 v[22:25], v[172:175], v[210:213], v[22:25]
	v_mfma_f32_16x16x32_bf16 v[18:21], v[184:187], v[210:213], v[18:21]
	v_mfma_f32_16x16x32_bf16 v[6:9], v[172:175], v[218:221], v[6:9]
	v_mfma_f32_16x16x32_bf16 v[2:5], v[184:187], v[218:221], v[2:5]
	v_mfma_f32_16x16x32_bf16 v[66:69], v[188:191], v[196:199], v[34:37]
	v_mfma_f32_16x16x32_bf16 v[22:25], v[180:183], v[214:217], v[22:25]
	v_mfma_f32_16x16x32_bf16 v[18:21], v[188:191], v[214:217], v[18:21]
	v_mfma_f32_16x16x32_bf16 v[6:9], v[180:183], v[222:225], v[6:9]
	v_mfma_f32_16x16x32_bf16 v[2:5], v[188:191], v[222:225], v[2:5]
	s_setprio 0
	s_barrier
	s_add_u32 s52, s52, 0x100
	s_addc_u32 s53, s53, 0
	s_add_u32 s67, s67, 0x100
	s_addc_u32 s68, s68, 0
	s_cmp_ge_i32 s69, s58
	s_mov_b32 s54, s69
	s_cbranch_scc0 .LBB0_1873

.LBB0_1953:
	s_add_i32 s44, s40, 2
	s_add_u32 s7, s38, 0x80
	s_addc_u32 s10, s39, 0
	s_add_i32 s45, 0, 0x10000
	s_cmp_eq_u32 s74, s40
	s_cselect_b32 s41, s65, s10
	s_cselect_b32 s40, s64, s7
	v_add_u32_e32 v0, s45, v247
	s_cselect_b32 s11, s67, s43
	s_cselect_b32 s10, s66, s42
	s_add_i32 s7, 0, 0x14000
	ds_read_b128 v[18:21], v0
	ds_read_b128 v[22:25], v0 offset:1024
	ds_read_b128 v[26:29], v0 offset:2048
	ds_read_b128 v[30:33], v0 offset:3072
	v_add_u32_e32 v0, s7, v247
	ds_read_b128 v[42:45], v0
	ds_read_b128 v[46:49], v0 offset:1024
	ds_read_b128 v[58:61], v0 offset:2048
	ds_read_b128 v[62:65], v0 offset:3072
	v_lshl_add_u64 v[202:203], s[38:39], 0, v[198:199]
	s_add_i32 m0, s17, 0xc000
	ds_read_b128 v[122:125], v248
	ds_read_b128 v[134:137], v248 offset:1024
	ds_read_b128 v[146:149], v248 offset:2048
	ds_read_b128 v[158:161], v248 offset:3072
	ds_read_b128 v[170:173], v248 offset:4096
	ds_read_b128 v[182:185], v248 offset:5120
	ds_read_b128 v[186:189], v248 offset:6144
	ds_read_b128 v[210:213], v248 offset:7168
	global_load_lds_dwordx4 v[202:203], off
	v_lshl_add_u64 v[202:203], s[38:39], 0, v[200:201]
	s_add_i32 m0, s17, 0xe000
	s_nop 0
	global_load_lds_dwordx4 v[202:203], off
	s_waitcnt vmcnt(8)
	s_waitcnt lgkmcnt(0)
	s_setprio 1
	s_barrier
	v_mfma_f32_16x16x32_bf16 v[174:177], v[18:21], v[122:125], v[174:177]
	v_mfma_f32_16x16x32_bf16 v[178:181], v[26:29], v[122:125], v[178:181]
	v_mfma_f32_16x16x32_bf16 v[154:157], v[18:21], v[146:149], v[154:157]
	v_mfma_f32_16x16x32_bf16 v[150:153], v[26:29], v[146:149], v[150:153]
	v_mfma_f32_16x16x32_bf16 v[130:133], v[18:21], v[170:173], v[130:133]
	v_mfma_f32_16x16x32_bf16 v[126:129], v[26:29], v[170:173], v[126:129]
	v_mfma_f32_16x16x32_bf16 v[110:113], v[18:21], v[186:189], v[110:113]
	v_mfma_f32_16x16x32_bf16 v[106:109], v[26:29], v[186:189], v[106:109]
	v_mfma_f32_16x16x32_bf16 v[174:177], v[22:25], v[134:137], v[174:177]
	v_mfma_f32_16x16x32_bf16 v[178:181], v[30:33], v[134:137], v[178:181]
	v_mfma_f32_16x16x32_bf16 v[154:157], v[22:25], v[158:161], v[154:157]
	v_mfma_f32_16x16x32_bf16 v[150:153], v[30:33], v[158:161], v[150:153]
	v_mfma_f32_16x16x32_bf16 v[130:133], v[22:25], v[182:185], v[130:133]
	v_mfma_f32_16x16x32_bf16 v[126:129], v[30:33], v[182:185], v[126:129]
	v_mfma_f32_16x16x32_bf16 v[110:113], v[22:25], v[210:213], v[110:113]
	v_mfma_f32_16x16x32_bf16 v[106:109], v[30:33], v[210:213], v[106:109]
	s_setprio 0
	s_setprio 1
	v_mfma_f32_16x16x32_bf16 v[166:169], v[42:45], v[122:125], v[166:169]
	v_mfma_f32_16x16x32_bf16 v[122:125], v[58:61], v[122:125], v[162:165]
	v_mfma_f32_16x16x32_bf16 v[138:141], v[58:61], v[146:149], v[138:141]
	v_mfma_f32_16x16x32_bf16 v[118:121], v[42:45], v[170:173], v[118:121]
	v_mfma_f32_16x16x32_bf16 v[114:117], v[58:61], v[170:173], v[114:117]
	v_mfma_f32_16x16x32_bf16 v[102:105], v[42:45], v[186:189], v[102:105]
	v_mfma_f32_16x16x32_bf16 v[98:101], v[58:61], v[186:189], v[98:101]
	v_mfma_f32_16x16x32_bf16 v[166:169], v[46:49], v[134:137], v[166:169]
	v_mfma_f32_16x16x32_bf16 v[122:125], v[62:65], v[134:137], v[122:125]
	v_mfma_f32_16x16x32_bf16 v[134:137], v[42:45], v[146:149], v[142:145]
	v_mfma_f32_16x16x32_bf16 v[138:141], v[62:65], v[158:161], v[138:141]
	v_mfma_f32_16x16x32_bf16 v[118:121], v[46:49], v[182:185], v[118:121]
	v_mfma_f32_16x16x32_bf16 v[114:117], v[62:65], v[182:185], v[114:117]
	v_mfma_f32_16x16x32_bf16 v[102:105], v[46:49], v[210:213], v[102:105]
	v_mfma_f32_16x16x32_bf16 v[98:101], v[62:65], v[210:213], v[98:101]
	v_mfma_f32_16x16x32_bf16 v[134:137], v[46:49], v[158:161], v[134:137]
	s_setprio 0
	s_barrier
	s_add_i32 s45, s45, s16
	v_lshl_add_u64 v[202:203], s[10:11], 0, v[192:193]
	s_mov_b32 m0, s45
	ds_read_b128 v[142:145], v248 offset:16384
	ds_read_b128 v[146:149], v248 offset:17408
	ds_read_b128 v[158:161], v248 offset:18432
	ds_read_b128 v[162:165], v248 offset:19456
	ds_read_b128 v[170:173], v248 offset:20480
	ds_read_b128 v[182:185], v248 offset:21504
	ds_read_b128 v[186:189], v248 offset:22528
	ds_read_b128 v[210:213], v248 offset:23552
	global_load_lds_dwordx4 v[202:203], off
	s_add_i32 m0, s45, 0x2000
	v_lshl_add_u64 v[222:223], s[10:11], 0, v[196:197]
	s_add_u32 s10, s10, s0
	s_addc_u32 s11, s11, s1
	s_add_i32 s7, s7, s16
	global_load_lds_dwordx4 v[222:223], off
	v_lshl_add_u64 v[224:225], s[10:11], 0, v[192:193]
	s_mov_b32 m0, s7
	v_lshl_add_u64 v[226:227], s[10:11], 0, v[196:197]
	global_load_lds_dwordx4 v[224:225], off
	s_add_i32 m0, s7, 0x2000
	v_lshl_add_u64 v[228:229], s[40:41], 0, v[190:191]
	global_load_lds_dwordx4 v[226:227], off
	s_mov_b32 m0, s17
	v_lshl_add_u64 v[230:231], s[40:41], 0, v[194:195]
	global_load_lds_dwordx4 v[228:229], off
	s_mov_b32 m0, s23
	s_nop 0
	global_load_lds_dwordx4 v[230:231], off
	s_waitcnt vmcnt(8)
	s_waitcnt lgkmcnt(0)
	s_setprio 1
	s_barrier
	v_mfma_f32_16x16x32_bf16 v[94:97], v[18:21], v[142:145], v[94:97]
	v_mfma_f32_16x16x32_bf16 v[90:93], v[26:29], v[142:145], v[90:93]
	v_mfma_f32_16x16x32_bf16 v[78:81], v[18:21], v[158:161], v[78:81]
	v_mfma_f32_16x16x32_bf16 v[74:77], v[26:29], v[158:161], v[74:77]
	v_mfma_f32_16x16x32_bf16 v[54:57], v[18:21], v[170:173], v[54:57]
	v_mfma_f32_16x16x32_bf16 v[50:53], v[26:29], v[170:173], v[50:53]
	v_mfma_f32_16x16x32_bf16 v[14:17], v[18:21], v[186:189], v[14:17]
	v_mfma_f32_16x16x32_bf16 v[10:13], v[26:29], v[186:189], v[10:13]
	v_mfma_f32_16x16x32_bf16 v[94:97], v[22:25], v[146:149], v[94:97]
	v_mfma_f32_16x16x32_bf16 v[90:93], v[30:33], v[146:149], v[90:93]
	v_mfma_f32_16x16x32_bf16 v[78:81], v[22:25], v[162:165], v[78:81]
	v_mfma_f32_16x16x32_bf16 v[74:77], v[30:33], v[162:165], v[74:77]
	v_mfma_f32_16x16x32_bf16 v[54:57], v[22:25], v[182:185], v[54:57]
	v_mfma_f32_16x16x32_bf16 v[50:53], v[30:33], v[182:185], v[50:53]
	v_mfma_f32_16x16x32_bf16 v[14:17], v[22:25], v[210:213], v[14:17]
	v_mfma_f32_16x16x32_bf16 v[10:13], v[30:33], v[210:213], v[10:13]
	s_setprio 0
	s_setprio 1
	v_mfma_f32_16x16x32_bf16 v[38:41], v[42:45], v[170:173], v[38:41]
	v_mfma_f32_16x16x32_bf16 v[34:37], v[58:61], v[170:173], v[34:37]
	v_mfma_f32_16x16x32_bf16 v[6:9], v[42:45], v[186:189], v[6:9]
	v_mfma_f32_16x16x32_bf16 v[2:5], v[58:61], v[186:189], v[2:5]
	v_mfma_f32_16x16x32_bf16 v[18:21], v[42:45], v[142:145], v[86:89]
	v_mfma_f32_16x16x32_bf16 v[22:25], v[58:61], v[142:145], v[82:85]
	v_mfma_f32_16x16x32_bf16 v[26:29], v[42:45], v[158:161], v[70:73]
	v_mfma_f32_16x16x32_bf16 v[30:33], v[58:61], v[158:161], v[66:69]
	v_mfma_f32_16x16x32_bf16 v[38:41], v[46:49], v[182:185], v[38:41]
	v_mfma_f32_16x16x32_bf16 v[34:37], v[62:65], v[182:185], v[34:37]
	v_mfma_f32_16x16x32_bf16 v[6:9], v[46:49], v[210:213], v[6:9]
	v_mfma_f32_16x16x32_bf16 v[2:5], v[62:65], v[210:213], v[2:5]
	v_mfma_f32_16x16x32_bf16 v[18:21], v[46:49], v[146:149], v[18:21]
	v_mfma_f32_16x16x32_bf16 v[22:25], v[62:65], v[146:149], v[22:25]
	v_mfma_f32_16x16x32_bf16 v[26:29], v[46:49], v[162:165], v[26:29]
	v_mfma_f32_16x16x32_bf16 v[30:33], v[62:65], v[162:165], v[30:33]
	s_setprio 0
	s_barrier
	s_add_i32 s7, 0, 0x18000
	v_add_u32_e32 v0, s7, v247
	s_add_i32 s45, 0, 0x1c000
	ds_read_b128 v[42:45], v0
	ds_read_b128 v[46:49], v0 offset:1024
	ds_read_b128 v[58:61], v0 offset:2048
	ds_read_b128 v[62:65], v0 offset:3072
	v_add_u32_e32 v0, s45, v247
	ds_read_b128 v[146:149], v0
	ds_read_b128 v[158:161], v0 offset:1024
	ds_read_b128 v[170:173], v0 offset:2048
	ds_read_b128 v[182:185], v0 offset:3072
	s_add_u32 s10, s40, s0
	s_addc_u32 s11, s41, s1
	s_mov_b32 m0, s68
	v_lshl_add_u64 v[142:143], s[10:11], 0, v[190:191]
	ds_read_b128 v[66:69], v248 offset:32768
	ds_read_b128 v[70:73], v248 offset:33792
	ds_read_b128 v[82:85], v248 offset:34816
	ds_read_b128 v[86:89], v248 offset:35840
	ds_read_b128 v[186:189], v248 offset:36864
	ds_read_b128 v[210:213], v248 offset:37888
	ds_read_b128 v[214:217], v248 offset:38912
	ds_read_b128 v[218:221], v248 offset:39936
	global_load_lds_dwordx4 v[142:143], off
	v_lshl_add_u64 v[142:143], s[10:11], 0, v[194:195]
	s_mov_b32 m0, s69
	s_nop 0
	global_load_lds_dwordx4 v[142:143], off
	s_waitcnt vmcnt(8)
	s_waitcnt lgkmcnt(0)
	s_setprio 1
	s_barrier
	v_mfma_f32_16x16x32_bf16 v[142:145], v[42:45], v[66:69], v[174:177]
	v_mfma_f32_16x16x32_bf16 v[174:177], v[46:49], v[70:73], v[142:145]
	v_mfma_f32_16x16x32_bf16 v[142:145], v[58:61], v[66:69], v[178:181]
	v_mfma_f32_16x16x32_bf16 v[178:181], v[62:65], v[70:73], v[142:145]
	v_mfma_f32_16x16x32_bf16 v[142:145], v[42:45], v[82:85], v[154:157]
	v_mfma_f32_16x16x32_bf16 v[154:157], v[46:49], v[86:89], v[142:145]
	v_mfma_f32_16x16x32_bf16 v[142:145], v[58:61], v[82:85], v[150:153]
	v_mfma_f32_16x16x32_bf16 v[130:133], v[42:45], v[186:189], v[130:133]
	v_mfma_f32_16x16x32_bf16 v[126:129], v[58:61], v[186:189], v[126:129]
	v_mfma_f32_16x16x32_bf16 v[110:113], v[42:45], v[214:217], v[110:113]
	v_mfma_f32_16x16x32_bf16 v[106:109], v[58:61], v[214:217], v[106:109]
	v_mfma_f32_16x16x32_bf16 v[150:153], v[62:65], v[86:89], v[142:145]
	v_mfma_f32_16x16x32_bf16 v[130:133], v[46:49], v[210:213], v[130:133]
	v_mfma_f32_16x16x32_bf16 v[126:129], v[62:65], v[210:213], v[126:129]
	v_mfma_f32_16x16x32_bf16 v[110:113], v[46:49], v[218:221], v[110:113]
	v_mfma_f32_16x16x32_bf16 v[106:109], v[62:65], v[218:221], v[106:109]
	s_setprio 0
	s_setprio 1
	v_mfma_f32_16x16x32_bf16 v[142:145], v[146:149], v[66:69], v[166:169]
	v_mfma_f32_16x16x32_bf16 v[66:69], v[170:173], v[66:69], v[122:125]
	v_mfma_f32_16x16x32_bf16 v[162:165], v[182:185], v[70:73], v[66:69]
	v_mfma_f32_16x16x32_bf16 v[66:69], v[146:149], v[82:85], v[134:137]
	v_mfma_f32_16x16x32_bf16 v[166:169], v[158:161], v[70:73], v[142:145]
	v_mfma_f32_16x16x32_bf16 v[142:145], v[158:161], v[86:89], v[66:69]
	v_mfma_f32_16x16x32_bf16 v[66:69], v[170:173], v[82:85], v[138:141]
	v_mfma_f32_16x16x32_bf16 v[138:141], v[182:185], v[86:89], v[66:69]
	v_mfma_f32_16x16x32_bf16 v[66:69], v[146:149], v[186:189], v[118:121]
	v_mfma_f32_16x16x32_bf16 v[118:121], v[158:161], v[210:213], v[66:69]
	v_mfma_f32_16x16x32_bf16 v[66:69], v[170:173], v[186:189], v[114:117]
	v_mfma_f32_16x16x32_bf16 v[114:117], v[182:185], v[210:213], v[66:69]
	v_mfma_f32_16x16x32_bf16 v[66:69], v[146:149], v[214:217], v[102:105]
	v_mfma_f32_16x16x32_bf16 v[102:105], v[158:161], v[218:221], v[66:69]
	v_mfma_f32_16x16x32_bf16 v[66:69], v[170:173], v[214:217], v[98:101]
	v_mfma_f32_16x16x32_bf16 v[98:101], v[182:185], v[218:221], v[66:69]
	s_setprio 0
	s_barrier
	s_add_i32 s7, s7, s16
	v_lshl_add_u64 v[82:83], v[202:203], 0, s[14:15]
	s_mov_b32 m0, s7
	s_nop 1
	ds_read_b128 v[66:69], v248 offset:49152
	ds_read_b128 v[70:73], v248 offset:50176
	ds_read_b128 v[122:125], v248 offset:51200
	ds_read_b128 v[134:137], v248 offset:52224
	ds_read_b128 v[186:189], v248 offset:53248
	ds_read_b128 v[210:213], v248 offset:54272
	ds_read_b128 v[214:217], v248 offset:55296
	ds_read_b128 v[218:221], v248 offset:56320
	global_load_lds_dwordx4 v[82:83], off
	v_lshl_add_u64 v[82:83], v[222:223], 0, s[14:15]
	s_add_i32 m0, s7, 0x2000
	s_add_i32 s7, s45, s16
	global_load_lds_dwordx4 v[82:83], off
	v_lshl_add_u64 v[82:83], v[224:225], 0, s[14:15]
	s_mov_b32 m0, s7
	s_nop 0
	global_load_lds_dwordx4 v[82:83], off
	v_lshl_add_u64 v[82:83], v[226:227], 0, s[14:15]
	s_add_i32 m0, s7, 0x2000
	s_nop 0
	global_load_lds_dwordx4 v[82:83], off
	v_lshl_add_u64 v[82:83], v[228:229], 0, s[14:15]
	s_mov_b32 m0, s8
	s_nop 0
	global_load_lds_dwordx4 v[82:83], off
	v_lshl_add_u64 v[82:83], v[230:231], 0, s[14:15]
	s_mov_b32 m0, s70
	s_nop 0
	global_load_lds_dwordx4 v[82:83], off
	s_waitcnt vmcnt(8)
	s_waitcnt lgkmcnt(0)
	s_setprio 1
	s_barrier
	v_mfma_f32_16x16x32_bf16 v[82:85], v[42:45], v[66:69], v[94:97]
	v_mfma_f32_16x16x32_bf16 v[94:97], v[46:49], v[70:73], v[82:85]
	v_mfma_f32_16x16x32_bf16 v[82:85], v[58:61], v[66:69], v[90:93]
	v_mfma_f32_16x16x32_bf16 v[78:81], v[42:45], v[122:125], v[78:81]
	v_mfma_f32_16x16x32_bf16 v[74:77], v[58:61], v[122:125], v[74:77]
	v_mfma_f32_16x16x32_bf16 v[54:57], v[42:45], v[186:189], v[54:57]
	v_mfma_f32_16x16x32_bf16 v[50:53], v[58:61], v[186:189], v[50:53]
	v_mfma_f32_16x16x32_bf16 v[14:17], v[42:45], v[214:217], v[14:17]
	v_mfma_f32_16x16x32_bf16 v[10:13], v[58:61], v[214:217], v[10:13]
	v_mfma_f32_16x16x32_bf16 v[90:93], v[62:65], v[70:73], v[82:85]
	v_mfma_f32_16x16x32_bf16 v[78:81], v[46:49], v[134:137], v[78:81]
	v_mfma_f32_16x16x32_bf16 v[74:77], v[62:65], v[134:137], v[74:77]
	v_mfma_f32_16x16x32_bf16 v[54:57], v[46:49], v[210:213], v[54:57]
	v_mfma_f32_16x16x32_bf16 v[50:53], v[62:65], v[210:213], v[50:53]
	v_mfma_f32_16x16x32_bf16 v[14:17], v[46:49], v[218:221], v[14:17]
	v_mfma_f32_16x16x32_bf16 v[10:13], v[62:65], v[218:221], v[10:13]
	s_setprio 0
	s_setprio 1
	v_mfma_f32_16x16x32_bf16 v[18:21], v[146:149], v[66:69], v[18:21]
	v_mfma_f32_16x16x32_bf16 v[86:89], v[158:161], v[70:73], v[18:21]
	v_mfma_f32_16x16x32_bf16 v[18:21], v[170:173], v[66:69], v[22:25]
	v_mfma_f32_16x16x32_bf16 v[82:85], v[182:185], v[70:73], v[18:21]
	v_mfma_f32_16x16x32_bf16 v[18:21], v[146:149], v[122:125], v[26:29]
	v_mfma_f32_16x16x32_bf16 v[70:73], v[158:161], v[134:137], v[18:21]
	v_mfma_f32_16x16x32_bf16 v[18:21], v[170:173], v[122:125], v[30:33]
	v_mfma_f32_16x16x32_bf16 v[66:69], v[182:185], v[134:137], v[18:21]
	v_mfma_f32_16x16x32_bf16 v[18:21], v[146:149], v[186:189], v[38:41]
	v_mfma_f32_16x16x32_bf16 v[38:41], v[158:161], v[210:213], v[18:21]
	v_mfma_f32_16x16x32_bf16 v[18:21], v[170:173], v[186:189], v[34:37]
	v_mfma_f32_16x16x32_bf16 v[6:9], v[146:149], v[214:217], v[6:9]
	v_mfma_f32_16x16x32_bf16 v[2:5], v[170:173], v[214:217], v[2:5]
	v_mfma_f32_16x16x32_bf16 v[34:37], v[182:185], v[210:213], v[18:21]
	v_mfma_f32_16x16x32_bf16 v[6:9], v[158:161], v[218:221], v[6:9]
	v_mfma_f32_16x16x32_bf16 v[2:5], v[182:185], v[218:221], v[2:5]
	s_setprio 0
	s_barrier
	s_add_u32 s38, s38, 0x100
	s_addc_u32 s39, s39, 0
	s_add_u32 s42, s42, 0x100
	s_addc_u32 s43, s43, 0
	s_cmp_ge_i32 s44, s71
	s_mov_b32 s40, s44
	s_cbranch_scc0 .LBB0_1953
